# hand-written radix top-k select in indexer (P2b)
# speedup vs baseline: 1.0113x; 1.0113x over previous
.LBB0_580:
	v_mov_b32_e32 v2, v0
	s_nop 0
	v_readfirstlane_b32 s0, v2
	s_bfe_u32 s14, s0, 0x30006
	s_lshl_b32 s0, s4, 4
	s_lshl_b32 s1, s14, 1
	s_or_b32 s92, s1, s0
	s_or_b32 s22, s92, 1
	s_add_i32 s31, s92, 2
	v_and_b32_e32 v146, 63, v2
	s_cmpk_gt_u32 s92, 0xfe
	s_mov_b64 s[0:1], -1
	s_cbranch_scc0 .LBB0_602
	s_lshl_b32 s2, s14, 14
	v_lshl_add_u32 v7, v146, 2, s2
	s_lshr_b32 s3, s92, 6
	s_mul_i32 s5, s14, 0xa00
	s_add_i32 s5, s5, 0x20000
	s_add_i32 s6, s5, 0x500
	v_mov_b32_e32 v199, 1
	v_mov_b32_e32 v248, 0
	v_mov_b32_e32 v249, 0
	v_mov_b32_e32 v250, 0
	v_mov_b32_e32 v251, 0
	v_mov_b32_e32 v2, 0
	v_mov_b32_e32 v3, 0
	v_mov_b32_e32 v4, 0
	v_mov_b32_e32 v5, 0
	v_lshl_add_u32 v195, v146, 4, s5
	v_add_u32_e32 v247, 0x100, v146
	v_lshl_add_u32 v197, v146, 4, s2
	v_and_b32_e32 v188, 7, v146
	v_lshl_add_u32 v188, v188, 10, s2
	v_add_u32_e32 v189, 0x2000, v188
	s_mov_b32 s7, 0
	s_mov_b32 s8, 0
	s_movk_i32 s9, 0x100
	s_movk_i32 s10, 0x100
	s_mov_b32 s12, 0
	s_mov_b32 s13, 0
	ds_read2st64_b32 v[200:201], v7 offset0:0 offset1:1
	ds_read2st64_b32 v[202:203], v7 offset0:2 offset1:3
	ds_read2st64_b32 v[148:149], v7 offset0:32 offset1:33
	ds_read2st64_b32 v[150:151], v7 offset0:34 offset1:35
	s_waitcnt lgkmcnt(3)
	v_ashrrev_i32_e32 v9, 31, v200
	v_bitop3_b32 v200, v9, v200, s30 bitop3:0x36
	v_ashrrev_i32_e32 v10, 31, v201
	v_bitop3_b32 v201, v10, v201, s30 bitop3:0x36
	s_waitcnt lgkmcnt(2)
	v_ashrrev_i32_e32 v11, 31, v202
	v_bitop3_b32 v202, v11, v202, s30 bitop3:0x36
	v_ashrrev_i32_e32 v12, 31, v203
	v_bitop3_b32 v203, v12, v203, s30 bitop3:0x36
	s_waitcnt lgkmcnt(1)
	v_ashrrev_i32_e32 v9, 31, v148
	v_bitop3_b32 v148, v9, v148, s30 bitop3:0x36
	v_ashrrev_i32_e32 v10, 31, v149
	v_bitop3_b32 v149, v10, v149, s30 bitop3:0x36
	s_waitcnt lgkmcnt(0)
	v_ashrrev_i32_e32 v11, 31, v150
	v_bitop3_b32 v150, v11, v150, s30 bitop3:0x36
	v_ashrrev_i32_e32 v12, 31, v151
	v_bitop3_b32 v151, v12, v151, s30 bitop3:0x36
	ds_read2st64_b32 v[204:205], v7 offset0:4 offset1:5
	ds_read2st64_b32 v[206:207], v7 offset0:6 offset1:7
	ds_read2st64_b32 v[152:153], v7 offset0:36 offset1:37
	ds_read2st64_b32 v[154:155], v7 offset0:38 offset1:39
	s_waitcnt lgkmcnt(3)
	v_ashrrev_i32_e32 v9, 31, v204
	v_bitop3_b32 v204, v9, v204, s30 bitop3:0x36
	v_ashrrev_i32_e32 v10, 31, v205
	v_bitop3_b32 v205, v10, v205, s30 bitop3:0x36
	s_waitcnt lgkmcnt(2)
	v_ashrrev_i32_e32 v11, 31, v206
	v_bitop3_b32 v206, v11, v206, s30 bitop3:0x36
	v_ashrrev_i32_e32 v12, 31, v207
	v_bitop3_b32 v207, v12, v207, s30 bitop3:0x36
	s_waitcnt lgkmcnt(1)
	v_ashrrev_i32_e32 v9, 31, v152
	v_bitop3_b32 v152, v9, v152, s30 bitop3:0x36
	v_ashrrev_i32_e32 v10, 31, v153
	v_bitop3_b32 v153, v10, v153, s30 bitop3:0x36
	s_waitcnt lgkmcnt(0)
	v_ashrrev_i32_e32 v11, 31, v154
	v_bitop3_b32 v154, v11, v154, s30 bitop3:0x36
	v_ashrrev_i32_e32 v12, 31, v155
	v_bitop3_b32 v155, v12, v155, s30 bitop3:0x36
	s_cmp_lt_u32 s3, 8
	s_cbranch_scc1 .Lsel_fix1_3
	ds_read2st64_b32 v[208:209], v7 offset0:8 offset1:9
	ds_read2st64_b32 v[210:211], v7 offset0:10 offset1:11
	ds_read2st64_b32 v[156:157], v7 offset0:40 offset1:41
	ds_read2st64_b32 v[158:159], v7 offset0:42 offset1:43
	s_waitcnt lgkmcnt(3)
	v_ashrrev_i32_e32 v9, 31, v208
	v_bitop3_b32 v208, v9, v208, s30 bitop3:0x36
	v_ashrrev_i32_e32 v10, 31, v209
	v_bitop3_b32 v209, v10, v209, s30 bitop3:0x36
	s_waitcnt lgkmcnt(2)
	v_ashrrev_i32_e32 v11, 31, v210
	v_bitop3_b32 v210, v11, v210, s30 bitop3:0x36
	v_ashrrev_i32_e32 v12, 31, v211
	v_bitop3_b32 v211, v12, v211, s30 bitop3:0x36
	s_waitcnt lgkmcnt(1)
	v_ashrrev_i32_e32 v9, 31, v156
	v_bitop3_b32 v156, v9, v156, s30 bitop3:0x36
	v_ashrrev_i32_e32 v10, 31, v157
	v_bitop3_b32 v157, v10, v157, s30 bitop3:0x36
	s_waitcnt lgkmcnt(0)
	v_ashrrev_i32_e32 v11, 31, v158
	v_bitop3_b32 v158, v11, v158, s30 bitop3:0x36
	v_ashrrev_i32_e32 v12, 31, v159
	v_bitop3_b32 v159, v12, v159, s30 bitop3:0x36
	s_cmp_lt_u32 s3, 12
	s_cbranch_scc1 .Lsel_fix2_4
	ds_read2st64_b32 v[212:213], v7 offset0:12 offset1:13
	ds_read2st64_b32 v[214:215], v7 offset0:14 offset1:15
	ds_read2st64_b32 v[160:161], v7 offset0:44 offset1:45
	ds_read2st64_b32 v[162:163], v7 offset0:46 offset1:47
	s_waitcnt lgkmcnt(3)
	v_ashrrev_i32_e32 v9, 31, v212
	v_bitop3_b32 v212, v9, v212, s30 bitop3:0x36
	v_ashrrev_i32_e32 v10, 31, v213
	v_bitop3_b32 v213, v10, v213, s30 bitop3:0x36
	s_waitcnt lgkmcnt(2)
	v_ashrrev_i32_e32 v11, 31, v214
	v_bitop3_b32 v214, v11, v214, s30 bitop3:0x36
	v_ashrrev_i32_e32 v12, 31, v215
	v_bitop3_b32 v215, v12, v215, s30 bitop3:0x36
	s_waitcnt lgkmcnt(1)
	v_ashrrev_i32_e32 v9, 31, v160
	v_bitop3_b32 v160, v9, v160, s30 bitop3:0x36
	v_ashrrev_i32_e32 v10, 31, v161
	v_bitop3_b32 v161, v10, v161, s30 bitop3:0x36
	s_waitcnt lgkmcnt(0)
	v_ashrrev_i32_e32 v11, 31, v162
	v_bitop3_b32 v162, v11, v162, s30 bitop3:0x36
	v_ashrrev_i32_e32 v12, 31, v163
	v_bitop3_b32 v163, v12, v163, s30 bitop3:0x36
	s_cmp_lt_u32 s3, 16
	s_cbranch_scc1 .Lsel_fix3_5
	ds_read2st64_b32 v[216:217], v7 offset0:16 offset1:17
	ds_read2st64_b32 v[218:219], v7 offset0:18 offset1:19
	ds_read2st64_b32 v[164:165], v7 offset0:48 offset1:49
	ds_read2st64_b32 v[166:167], v7 offset0:50 offset1:51
	s_waitcnt lgkmcnt(3)
	v_ashrrev_i32_e32 v9, 31, v216
	v_bitop3_b32 v216, v9, v216, s30 bitop3:0x36
	v_ashrrev_i32_e32 v10, 31, v217
	v_bitop3_b32 v217, v10, v217, s30 bitop3:0x36
	s_waitcnt lgkmcnt(2)
	v_ashrrev_i32_e32 v11, 31, v218
	v_bitop3_b32 v218, v11, v218, s30 bitop3:0x36
	v_ashrrev_i32_e32 v12, 31, v219
	v_bitop3_b32 v219, v12, v219, s30 bitop3:0x36
	s_waitcnt lgkmcnt(1)
	v_ashrrev_i32_e32 v9, 31, v164
	v_bitop3_b32 v164, v9, v164, s30 bitop3:0x36
	v_ashrrev_i32_e32 v10, 31, v165
	v_bitop3_b32 v165, v10, v165, s30 bitop3:0x36
	s_waitcnt lgkmcnt(0)
	v_ashrrev_i32_e32 v11, 31, v166
	v_bitop3_b32 v166, v11, v166, s30 bitop3:0x36
	v_ashrrev_i32_e32 v12, 31, v167
	v_bitop3_b32 v167, v12, v167, s30 bitop3:0x36
	s_cmp_lt_u32 s3, 20
	s_cbranch_scc1 .Lsel_fix4_6
	ds_read2st64_b32 v[220:221], v7 offset0:20 offset1:21
	ds_read2st64_b32 v[222:223], v7 offset0:22 offset1:23
	ds_read2st64_b32 v[168:169], v7 offset0:52 offset1:53
	ds_read2st64_b32 v[170:171], v7 offset0:54 offset1:55
	s_waitcnt lgkmcnt(3)
	v_ashrrev_i32_e32 v9, 31, v220
	v_bitop3_b32 v220, v9, v220, s30 bitop3:0x36
	v_ashrrev_i32_e32 v10, 31, v221
	v_bitop3_b32 v221, v10, v221, s30 bitop3:0x36
	s_waitcnt lgkmcnt(2)
	v_ashrrev_i32_e32 v11, 31, v222
	v_bitop3_b32 v222, v11, v222, s30 bitop3:0x36
	v_ashrrev_i32_e32 v12, 31, v223
	v_bitop3_b32 v223, v12, v223, s30 bitop3:0x36
	s_waitcnt lgkmcnt(1)
	v_ashrrev_i32_e32 v9, 31, v168
	v_bitop3_b32 v168, v9, v168, s30 bitop3:0x36
	v_ashrrev_i32_e32 v10, 31, v169
	v_bitop3_b32 v169, v10, v169, s30 bitop3:0x36
	s_waitcnt lgkmcnt(0)
	v_ashrrev_i32_e32 v11, 31, v170
	v_bitop3_b32 v170, v11, v170, s30 bitop3:0x36
	v_ashrrev_i32_e32 v12, 31, v171
	v_bitop3_b32 v171, v12, v171, s30 bitop3:0x36
	s_cmp_lt_u32 s3, 24
	s_cbranch_scc1 .Lsel_fix5_7
	ds_read2st64_b32 v[224:225], v7 offset0:24 offset1:25
	ds_read2st64_b32 v[226:227], v7 offset0:26 offset1:27
	ds_read2st64_b32 v[172:173], v7 offset0:56 offset1:57
	ds_read2st64_b32 v[174:175], v7 offset0:58 offset1:59
	s_waitcnt lgkmcnt(3)
	v_ashrrev_i32_e32 v9, 31, v224
	v_bitop3_b32 v224, v9, v224, s30 bitop3:0x36
	v_ashrrev_i32_e32 v10, 31, v225
	v_bitop3_b32 v225, v10, v225, s30 bitop3:0x36
	s_waitcnt lgkmcnt(2)
	v_ashrrev_i32_e32 v11, 31, v226
	v_bitop3_b32 v226, v11, v226, s30 bitop3:0x36
	v_ashrrev_i32_e32 v12, 31, v227
	v_bitop3_b32 v227, v12, v227, s30 bitop3:0x36
	s_waitcnt lgkmcnt(1)
	v_ashrrev_i32_e32 v9, 31, v172
	v_bitop3_b32 v172, v9, v172, s30 bitop3:0x36
	v_ashrrev_i32_e32 v10, 31, v173
	v_bitop3_b32 v173, v10, v173, s30 bitop3:0x36
	s_waitcnt lgkmcnt(0)
	v_ashrrev_i32_e32 v11, 31, v174
	v_bitop3_b32 v174, v11, v174, s30 bitop3:0x36
	v_ashrrev_i32_e32 v12, 31, v175
	v_bitop3_b32 v175, v12, v175, s30 bitop3:0x36
	s_cmp_lt_u32 s3, 28
	s_cbranch_scc1 .Lsel_fix6_8
	ds_read2st64_b32 v[228:229], v7 offset0:28 offset1:29
	ds_read2st64_b32 v[230:231], v7 offset0:30 offset1:31
	ds_read2st64_b32 v[176:177], v7 offset0:60 offset1:61
	ds_read2st64_b32 v[186:187], v7 offset0:62 offset1:63
	s_waitcnt lgkmcnt(3)
	v_ashrrev_i32_e32 v9, 31, v228
	v_bitop3_b32 v228, v9, v228, s30 bitop3:0x36
	v_ashrrev_i32_e32 v10, 31, v229
	v_bitop3_b32 v229, v10, v229, s30 bitop3:0x36
	s_waitcnt lgkmcnt(2)
	v_ashrrev_i32_e32 v11, 31, v230
	v_bitop3_b32 v230, v11, v230, s30 bitop3:0x36
	v_ashrrev_i32_e32 v12, 31, v231
	v_bitop3_b32 v231, v12, v231, s30 bitop3:0x36
	s_waitcnt lgkmcnt(1)
	v_ashrrev_i32_e32 v9, 31, v176
	v_bitop3_b32 v176, v9, v176, s30 bitop3:0x36
	v_ashrrev_i32_e32 v10, 31, v177
	v_bitop3_b32 v177, v10, v177, s30 bitop3:0x36
	s_waitcnt lgkmcnt(0)
	v_ashrrev_i32_e32 v11, 31, v186
	v_bitop3_b32 v186, v11, v186, s30 bitop3:0x36
	v_ashrrev_i32_e32 v12, 31, v187
	v_bitop3_b32 v187, v12, v187, s30 bitop3:0x36
	s_branch .Lsel_fix7_9
.Lsel_fix1_3:
	s_sub_i32 s20, s92, 256
	s_sub_i32 s21, s92, 320
	s_sub_i32 s22, s92, 384
	s_sub_i32 s23, s92, 448
	v_cmp_ge_i32_e64 s[58:59], s20, v146
	v_cmp_ge_i32_e64 s[60:61], s21, v146
	v_cmp_ge_i32_e64 s[62:63], s22, v146
	v_cmp_ge_i32_e64 s[68:69], s23, v146
	s_add_i32 s20, s20, 1
	s_add_i32 s21, s21, 1
	s_add_i32 s22, s22, 1
	s_add_i32 s23, s23, 1
	v_cmp_ge_i32_e64 s[70:71], s20, v146
	v_cmp_ge_i32_e64 s[72:73], s21, v146
	v_cmp_ge_i32_e64 s[74:75], s22, v146
	v_cmp_ge_i32_e64 s[76:77], s23, v146
	v_cndmask_b32_e64 v204, 0, v204, s[58:59]
	v_cndmask_b32_e64 v205, 0, v205, s[60:61]
	v_cndmask_b32_e64 v206, 0, v206, s[62:63]
	v_cndmask_b32_e64 v207, 0, v207, s[68:69]
	v_cndmask_b32_e64 v152, 0, v152, s[70:71]
	v_cndmask_b32_e64 v153, 0, v153, s[72:73]
	v_cndmask_b32_e64 v154, 0, v154, s[74:75]
	v_cndmask_b32_e64 v155, 0, v155, s[76:77]
	s_branch .Lsel_load_done_1
.Lsel_fix2_4:
	s_sub_i32 s20, s92, 512
	s_sub_i32 s21, s92, 576
	s_sub_i32 s22, s92, 640
	s_sub_i32 s23, s92, 704
	v_cmp_ge_i32_e64 s[58:59], s20, v146
	v_cmp_ge_i32_e64 s[60:61], s21, v146
	v_cmp_ge_i32_e64 s[62:63], s22, v146
	v_cmp_ge_i32_e64 s[68:69], s23, v146
	s_add_i32 s20, s20, 1
	s_add_i32 s21, s21, 1
	s_add_i32 s22, s22, 1
	s_add_i32 s23, s23, 1
	v_cmp_ge_i32_e64 s[70:71], s20, v146
	v_cmp_ge_i32_e64 s[72:73], s21, v146
	v_cmp_ge_i32_e64 s[74:75], s22, v146
	v_cmp_ge_i32_e64 s[76:77], s23, v146
	v_cndmask_b32_e64 v208, 0, v208, s[58:59]
	v_cndmask_b32_e64 v209, 0, v209, s[60:61]
	v_cndmask_b32_e64 v210, 0, v210, s[62:63]
	v_cndmask_b32_e64 v211, 0, v211, s[68:69]
	v_cndmask_b32_e64 v156, 0, v156, s[70:71]
	v_cndmask_b32_e64 v157, 0, v157, s[72:73]
	v_cndmask_b32_e64 v158, 0, v158, s[74:75]
	v_cndmask_b32_e64 v159, 0, v159, s[76:77]
	s_branch .Lsel_load_done_1
.Lsel_fix3_5:
	s_sub_i32 s20, s92, 768
	s_sub_i32 s21, s92, 832
	s_sub_i32 s22, s92, 896
	s_sub_i32 s23, s92, 960
	v_cmp_ge_i32_e64 s[58:59], s20, v146
	v_cmp_ge_i32_e64 s[60:61], s21, v146
	v_cmp_ge_i32_e64 s[62:63], s22, v146
	v_cmp_ge_i32_e64 s[68:69], s23, v146
	s_add_i32 s20, s20, 1
	s_add_i32 s21, s21, 1
	s_add_i32 s22, s22, 1
	s_add_i32 s23, s23, 1
	v_cmp_ge_i32_e64 s[70:71], s20, v146
	v_cmp_ge_i32_e64 s[72:73], s21, v146
	v_cmp_ge_i32_e64 s[74:75], s22, v146
	v_cmp_ge_i32_e64 s[76:77], s23, v146
	v_cndmask_b32_e64 v212, 0, v212, s[58:59]
	v_cndmask_b32_e64 v213, 0, v213, s[60:61]
	v_cndmask_b32_e64 v214, 0, v214, s[62:63]
	v_cndmask_b32_e64 v215, 0, v215, s[68:69]
	v_cndmask_b32_e64 v160, 0, v160, s[70:71]
	v_cndmask_b32_e64 v161, 0, v161, s[72:73]
	v_cndmask_b32_e64 v162, 0, v162, s[74:75]
	v_cndmask_b32_e64 v163, 0, v163, s[76:77]
	s_branch .Lsel_load_done_1
.Lsel_fix4_6:
	s_sub_i32 s20, s92, 1024
	s_sub_i32 s21, s92, 1088
	s_sub_i32 s22, s92, 1152
	s_sub_i32 s23, s92, 1216
	v_cmp_ge_i32_e64 s[58:59], s20, v146
	v_cmp_ge_i32_e64 s[60:61], s21, v146
	v_cmp_ge_i32_e64 s[62:63], s22, v146
	v_cmp_ge_i32_e64 s[68:69], s23, v146
	s_add_i32 s20, s20, 1
	s_add_i32 s21, s21, 1
	s_add_i32 s22, s22, 1
	s_add_i32 s23, s23, 1
	v_cmp_ge_i32_e64 s[70:71], s20, v146
	v_cmp_ge_i32_e64 s[72:73], s21, v146
	v_cmp_ge_i32_e64 s[74:75], s22, v146
	v_cmp_ge_i32_e64 s[76:77], s23, v146
	v_cndmask_b32_e64 v216, 0, v216, s[58:59]
	v_cndmask_b32_e64 v217, 0, v217, s[60:61]
	v_cndmask_b32_e64 v218, 0, v218, s[62:63]
	v_cndmask_b32_e64 v219, 0, v219, s[68:69]
	v_cndmask_b32_e64 v164, 0, v164, s[70:71]
	v_cndmask_b32_e64 v165, 0, v165, s[72:73]
	v_cndmask_b32_e64 v166, 0, v166, s[74:75]
	v_cndmask_b32_e64 v167, 0, v167, s[76:77]
	s_branch .Lsel_load_done_1
.Lsel_fix5_7:
	s_sub_i32 s20, s92, 1280
	s_sub_i32 s21, s92, 1344
	s_sub_i32 s22, s92, 1408
	s_sub_i32 s23, s92, 1472
	v_cmp_ge_i32_e64 s[58:59], s20, v146
	v_cmp_ge_i32_e64 s[60:61], s21, v146
	v_cmp_ge_i32_e64 s[62:63], s22, v146
	v_cmp_ge_i32_e64 s[68:69], s23, v146
	s_add_i32 s20, s20, 1
	s_add_i32 s21, s21, 1
	s_add_i32 s22, s22, 1
	s_add_i32 s23, s23, 1
	v_cmp_ge_i32_e64 s[70:71], s20, v146
	v_cmp_ge_i32_e64 s[72:73], s21, v146
	v_cmp_ge_i32_e64 s[74:75], s22, v146
	v_cmp_ge_i32_e64 s[76:77], s23, v146
	v_cndmask_b32_e64 v220, 0, v220, s[58:59]
	v_cndmask_b32_e64 v221, 0, v221, s[60:61]
	v_cndmask_b32_e64 v222, 0, v222, s[62:63]
	v_cndmask_b32_e64 v223, 0, v223, s[68:69]
	v_cndmask_b32_e64 v168, 0, v168, s[70:71]
	v_cndmask_b32_e64 v169, 0, v169, s[72:73]
	v_cndmask_b32_e64 v170, 0, v170, s[74:75]
	v_cndmask_b32_e64 v171, 0, v171, s[76:77]
	s_branch .Lsel_load_done_1
.Lsel_fix6_8:
	s_sub_i32 s20, s92, 1536
	s_sub_i32 s21, s92, 1600
	s_sub_i32 s22, s92, 1664
	s_sub_i32 s23, s92, 1728
	v_cmp_ge_i32_e64 s[58:59], s20, v146
	v_cmp_ge_i32_e64 s[60:61], s21, v146
	v_cmp_ge_i32_e64 s[62:63], s22, v146
	v_cmp_ge_i32_e64 s[68:69], s23, v146
	s_add_i32 s20, s20, 1
	s_add_i32 s21, s21, 1
	s_add_i32 s22, s22, 1
	s_add_i32 s23, s23, 1
	v_cmp_ge_i32_e64 s[70:71], s20, v146
	v_cmp_ge_i32_e64 s[72:73], s21, v146
	v_cmp_ge_i32_e64 s[74:75], s22, v146
	v_cmp_ge_i32_e64 s[76:77], s23, v146
	v_cndmask_b32_e64 v224, 0, v224, s[58:59]
	v_cndmask_b32_e64 v225, 0, v225, s[60:61]
	v_cndmask_b32_e64 v226, 0, v226, s[62:63]
	v_cndmask_b32_e64 v227, 0, v227, s[68:69]
	v_cndmask_b32_e64 v172, 0, v172, s[70:71]
	v_cndmask_b32_e64 v173, 0, v173, s[72:73]
	v_cndmask_b32_e64 v174, 0, v174, s[74:75]
	v_cndmask_b32_e64 v175, 0, v175, s[76:77]
	s_branch .Lsel_load_done_1
.Lsel_fix7_9:
	s_sub_i32 s20, s92, 1792
	s_sub_i32 s21, s92, 1856
	s_sub_i32 s22, s92, 1920
	s_sub_i32 s23, s92, 1984
	v_cmp_ge_i32_e64 s[58:59], s20, v146
	v_cmp_ge_i32_e64 s[60:61], s21, v146
	v_cmp_ge_i32_e64 s[62:63], s22, v146
	v_cmp_ge_i32_e64 s[68:69], s23, v146
	s_add_i32 s20, s20, 1
	s_add_i32 s21, s21, 1
	s_add_i32 s22, s22, 1
	s_add_i32 s23, s23, 1
	v_cmp_ge_i32_e64 s[70:71], s20, v146
	v_cmp_ge_i32_e64 s[72:73], s21, v146
	v_cmp_ge_i32_e64 s[74:75], s22, v146
	v_cmp_ge_i32_e64 s[76:77], s23, v146
	v_cndmask_b32_e64 v228, 0, v228, s[58:59]
	v_cndmask_b32_e64 v229, 0, v229, s[60:61]
	v_cndmask_b32_e64 v230, 0, v230, s[62:63]
	v_cndmask_b32_e64 v231, 0, v231, s[68:69]
	v_cndmask_b32_e64 v176, 0, v176, s[70:71]
	v_cndmask_b32_e64 v177, 0, v177, s[72:73]
	v_cndmask_b32_e64 v186, 0, v186, s[74:75]
	v_cndmask_b32_e64 v187, 0, v187, s[76:77]
.Lsel_load_done_1:
	ds_write_b128 v197, v[248:251] offset:0
	ds_write_b128 v197, v[248:251] offset:1024
	ds_write_b128 v197, v[248:251] offset:2048
	ds_write_b128 v197, v[248:251] offset:3072
	ds_write_b128 v197, v[248:251] offset:4096
	ds_write_b128 v197, v[248:251] offset:5120
	ds_write_b128 v197, v[248:251] offset:6144
	ds_write_b128 v197, v[248:251] offset:7168
	ds_write_b128 v197, v[248:251] offset:8192
	ds_write_b128 v197, v[248:251] offset:9216
	ds_write_b128 v197, v[248:251] offset:10240
	ds_write_b128 v197, v[248:251] offset:11264
	ds_write_b128 v197, v[248:251] offset:12288
	ds_write_b128 v197, v[248:251] offset:13312
	ds_write_b128 v197, v[248:251] offset:14336
	ds_write_b128 v197, v[248:251] offset:15360
	v_lshrrev_b32_e32 v9, 24, v200
	v_lshl_add_u32 v9, v9, 2, v188
	ds_add_u32 v9, v199
	v_lshrrev_b32_e32 v10, 24, v201
	v_lshl_add_u32 v10, v10, 2, v188
	ds_add_u32 v10, v199
	v_lshrrev_b32_e32 v11, 24, v202
	v_lshl_add_u32 v11, v11, 2, v188
	ds_add_u32 v11, v199
	v_lshrrev_b32_e32 v12, 24, v203
	v_lshl_add_u32 v12, v12, 2, v188
	ds_add_u32 v12, v199
	v_lshrrev_b32_e32 v13, 24, v148
	v_lshl_add_u32 v13, v13, 2, v189
	ds_add_u32 v13, v199
	v_lshrrev_b32_e32 v180, 24, v149
	v_lshl_add_u32 v180, v180, 2, v189
	ds_add_u32 v180, v199
	v_lshrrev_b32_e32 v182, 24, v150
	v_lshl_add_u32 v182, v182, 2, v189
	ds_add_u32 v182, v199
	v_lshrrev_b32_e32 v183, 24, v151
	v_lshl_add_u32 v183, v183, 2, v189
	ds_add_u32 v183, v199
	v_lshrrev_b32_e32 v9, 24, v204
	v_lshl_add_u32 v9, v9, 2, v188
	ds_add_u32 v9, v199
	v_lshrrev_b32_e32 v10, 24, v205
	v_lshl_add_u32 v10, v10, 2, v188
	ds_add_u32 v10, v199
	v_lshrrev_b32_e32 v11, 24, v206
	v_lshl_add_u32 v11, v11, 2, v188
	ds_add_u32 v11, v199
	v_lshrrev_b32_e32 v12, 24, v207
	v_lshl_add_u32 v12, v12, 2, v188
	ds_add_u32 v12, v199
	v_lshrrev_b32_e32 v13, 24, v152
	v_lshl_add_u32 v13, v13, 2, v189
	ds_add_u32 v13, v199
	v_lshrrev_b32_e32 v180, 24, v153
	v_lshl_add_u32 v180, v180, 2, v189
	ds_add_u32 v180, v199
	v_lshrrev_b32_e32 v182, 24, v154
	v_lshl_add_u32 v182, v182, 2, v189
	ds_add_u32 v182, v199
	v_lshrrev_b32_e32 v183, 24, v155
	v_lshl_add_u32 v183, v183, 2, v189
	ds_add_u32 v183, v199
	s_cmp_lt_u32 s3, 8
	s_cbranch_scc1 .Lsel_p1_done_10
	v_lshrrev_b32_e32 v9, 24, v208
	v_lshl_add_u32 v9, v9, 2, v188
	ds_add_u32 v9, v199
	v_lshrrev_b32_e32 v10, 24, v209
	v_lshl_add_u32 v10, v10, 2, v188
	ds_add_u32 v10, v199
	v_lshrrev_b32_e32 v11, 24, v210
	v_lshl_add_u32 v11, v11, 2, v188
	ds_add_u32 v11, v199
	v_lshrrev_b32_e32 v12, 24, v211
	v_lshl_add_u32 v12, v12, 2, v188
	ds_add_u32 v12, v199
	v_lshrrev_b32_e32 v13, 24, v156
	v_lshl_add_u32 v13, v13, 2, v189
	ds_add_u32 v13, v199
	v_lshrrev_b32_e32 v180, 24, v157
	v_lshl_add_u32 v180, v180, 2, v189
	ds_add_u32 v180, v199
	v_lshrrev_b32_e32 v182, 24, v158
	v_lshl_add_u32 v182, v182, 2, v189
	ds_add_u32 v182, v199
	v_lshrrev_b32_e32 v183, 24, v159
	v_lshl_add_u32 v183, v183, 2, v189
	ds_add_u32 v183, v199
	s_cmp_lt_u32 s3, 12
	s_cbranch_scc1 .Lsel_p1_done_10
	v_lshrrev_b32_e32 v9, 24, v212
	v_lshl_add_u32 v9, v9, 2, v188
	ds_add_u32 v9, v199
	v_lshrrev_b32_e32 v10, 24, v213
	v_lshl_add_u32 v10, v10, 2, v188
	ds_add_u32 v10, v199
	v_lshrrev_b32_e32 v11, 24, v214
	v_lshl_add_u32 v11, v11, 2, v188
	ds_add_u32 v11, v199
	v_lshrrev_b32_e32 v12, 24, v215
	v_lshl_add_u32 v12, v12, 2, v188
	ds_add_u32 v12, v199
	v_lshrrev_b32_e32 v13, 24, v160
	v_lshl_add_u32 v13, v13, 2, v189
	ds_add_u32 v13, v199
	v_lshrrev_b32_e32 v180, 24, v161
	v_lshl_add_u32 v180, v180, 2, v189
	ds_add_u32 v180, v199
	v_lshrrev_b32_e32 v182, 24, v162
	v_lshl_add_u32 v182, v182, 2, v189
	ds_add_u32 v182, v199
	v_lshrrev_b32_e32 v183, 24, v163
	v_lshl_add_u32 v183, v183, 2, v189
	ds_add_u32 v183, v199
	s_cmp_lt_u32 s3, 16
	s_cbranch_scc1 .Lsel_p1_done_10
	v_lshrrev_b32_e32 v9, 24, v216
	v_lshl_add_u32 v9, v9, 2, v188
	ds_add_u32 v9, v199
	v_lshrrev_b32_e32 v10, 24, v217
	v_lshl_add_u32 v10, v10, 2, v188
	ds_add_u32 v10, v199
	v_lshrrev_b32_e32 v11, 24, v218
	v_lshl_add_u32 v11, v11, 2, v188
	ds_add_u32 v11, v199
	v_lshrrev_b32_e32 v12, 24, v219
	v_lshl_add_u32 v12, v12, 2, v188
	ds_add_u32 v12, v199
	v_lshrrev_b32_e32 v13, 24, v164
	v_lshl_add_u32 v13, v13, 2, v189
	ds_add_u32 v13, v199
	v_lshrrev_b32_e32 v180, 24, v165
	v_lshl_add_u32 v180, v180, 2, v189
	ds_add_u32 v180, v199
	v_lshrrev_b32_e32 v182, 24, v166
	v_lshl_add_u32 v182, v182, 2, v189
	ds_add_u32 v182, v199
	v_lshrrev_b32_e32 v183, 24, v167
	v_lshl_add_u32 v183, v183, 2, v189
	ds_add_u32 v183, v199
	s_cmp_lt_u32 s3, 20
	s_cbranch_scc1 .Lsel_p1_done_10
	v_lshrrev_b32_e32 v9, 24, v220
	v_lshl_add_u32 v9, v9, 2, v188
	ds_add_u32 v9, v199
	v_lshrrev_b32_e32 v10, 24, v221
	v_lshl_add_u32 v10, v10, 2, v188
	ds_add_u32 v10, v199
	v_lshrrev_b32_e32 v11, 24, v222
	v_lshl_add_u32 v11, v11, 2, v188
	ds_add_u32 v11, v199
	v_lshrrev_b32_e32 v12, 24, v223
	v_lshl_add_u32 v12, v12, 2, v188
	ds_add_u32 v12, v199
	v_lshrrev_b32_e32 v13, 24, v168
	v_lshl_add_u32 v13, v13, 2, v189
	ds_add_u32 v13, v199
	v_lshrrev_b32_e32 v180, 24, v169
	v_lshl_add_u32 v180, v180, 2, v189
	ds_add_u32 v180, v199
	v_lshrrev_b32_e32 v182, 24, v170
	v_lshl_add_u32 v182, v182, 2, v189
	ds_add_u32 v182, v199
	v_lshrrev_b32_e32 v183, 24, v171
	v_lshl_add_u32 v183, v183, 2, v189
	ds_add_u32 v183, v199
	s_cmp_lt_u32 s3, 24
	s_cbranch_scc1 .Lsel_p1_done_10
	v_lshrrev_b32_e32 v9, 24, v224
	v_lshl_add_u32 v9, v9, 2, v188
	ds_add_u32 v9, v199
	v_lshrrev_b32_e32 v10, 24, v225
	v_lshl_add_u32 v10, v10, 2, v188
	ds_add_u32 v10, v199
	v_lshrrev_b32_e32 v11, 24, v226
	v_lshl_add_u32 v11, v11, 2, v188
	ds_add_u32 v11, v199
	v_lshrrev_b32_e32 v12, 24, v227
	v_lshl_add_u32 v12, v12, 2, v188
	ds_add_u32 v12, v199
	v_lshrrev_b32_e32 v13, 24, v172
	v_lshl_add_u32 v13, v13, 2, v189
	ds_add_u32 v13, v199
	v_lshrrev_b32_e32 v180, 24, v173
	v_lshl_add_u32 v180, v180, 2, v189
	ds_add_u32 v180, v199
	v_lshrrev_b32_e32 v182, 24, v174
	v_lshl_add_u32 v182, v182, 2, v189
	ds_add_u32 v182, v199
	v_lshrrev_b32_e32 v183, 24, v175
	v_lshl_add_u32 v183, v183, 2, v189
	ds_add_u32 v183, v199
	s_cmp_lt_u32 s3, 28
	s_cbranch_scc1 .Lsel_p1_done_10
	v_lshrrev_b32_e32 v9, 24, v228
	v_lshl_add_u32 v9, v9, 2, v188
	ds_add_u32 v9, v199
	v_lshrrev_b32_e32 v10, 24, v229
	v_lshl_add_u32 v10, v10, 2, v188
	ds_add_u32 v10, v199
	v_lshrrev_b32_e32 v11, 24, v230
	v_lshl_add_u32 v11, v11, 2, v188
	ds_add_u32 v11, v199
	v_lshrrev_b32_e32 v12, 24, v231
	v_lshl_add_u32 v12, v12, 2, v188
	ds_add_u32 v12, v199
	v_lshrrev_b32_e32 v13, 24, v176
	v_lshl_add_u32 v13, v13, 2, v189
	ds_add_u32 v13, v199
	v_lshrrev_b32_e32 v180, 24, v177
	v_lshl_add_u32 v180, v180, 2, v189
	ds_add_u32 v180, v199
	v_lshrrev_b32_e32 v182, 24, v186
	v_lshl_add_u32 v182, v182, 2, v189
	ds_add_u32 v182, v199
	v_lshrrev_b32_e32 v183, 24, v187
	v_lshl_add_u32 v183, v183, 2, v189
	ds_add_u32 v183, v199
.Lsel_p1_done_10:
	s_movk_i32 s11, 24
	s_waitcnt lgkmcnt(0)
	ds_read_b128 v[16:19], v197 offset:0
	ds_read_b128 v[20:23], v197 offset:1024
	ds_read_b128 v[24:27], v197 offset:2048
	ds_read_b128 v[28:31], v197 offset:3072
	ds_read_b128 v[190:193], v197 offset:4096
	ds_read_b128 v[10:13], v197 offset:5120
	ds_read_b128 v[180:183], v197 offset:6144
	ds_read_b128 v[6:9], v197 offset:7168
	s_waitcnt lgkmcnt(0)
	v_add3_u32 v232, v16, v20, v24
	v_add3_u32 v28, v28, v190, v10
	v_add3_u32 v232, v232, v180, v6
	v_add_u32_e32 v232, v232, v28
	v_add3_u32 v233, v17, v21, v25
	v_add3_u32 v29, v29, v191, v11
	v_add3_u32 v233, v233, v181, v7
	v_add_u32_e32 v233, v233, v29
	v_add3_u32 v234, v18, v22, v26
	v_add3_u32 v30, v30, v192, v12
	v_add3_u32 v234, v234, v182, v8
	v_add_u32_e32 v234, v234, v30
	v_add3_u32 v235, v19, v23, v27
	v_add3_u32 v31, v31, v193, v13
	v_add3_u32 v235, v235, v183, v9
	v_add_u32_e32 v235, v235, v31
	ds_read_b128 v[16:19], v197 offset:8192
	ds_read_b128 v[20:23], v197 offset:9216
	ds_read_b128 v[24:27], v197 offset:10240
	ds_read_b128 v[28:31], v197 offset:11264
	ds_read_b128 v[190:193], v197 offset:12288
	ds_read_b128 v[10:13], v197 offset:13312
	ds_read_b128 v[180:183], v197 offset:14336
	ds_read_b128 v[6:9], v197 offset:15360
	s_waitcnt lgkmcnt(0)
	v_add3_u32 v236, v16, v20, v24
	v_add3_u32 v28, v28, v190, v10
	v_add3_u32 v236, v236, v180, v6
	v_add_u32_e32 v236, v236, v28
	v_add3_u32 v237, v17, v21, v25
	v_add3_u32 v29, v29, v191, v11
	v_add3_u32 v237, v237, v181, v7
	v_add_u32_e32 v237, v237, v29
	v_add3_u32 v238, v18, v22, v26
	v_add3_u32 v30, v30, v192, v12
	v_add3_u32 v238, v238, v182, v8
	v_add_u32_e32 v238, v238, v30
	v_add3_u32 v239, v19, v23, v27
	v_add3_u32 v31, v31, v193, v13
	v_add3_u32 v239, v239, v183, v9
	v_add_u32_e32 v239, v239, v31
	v_add3_u32 v240, v232, v233, v234
	v_add3_u32 v241, v236, v237, v238
	v_add_u32_e32 v240, v240, v235
	v_add_u32_e32 v241, v241, v239
	v_lshl_add_u32 v242, v241, 16, v240
	s_nop 1
	v_add_u32_dpp v242, v242, v242 row_shr:1 row_mask:0xf bank_mask:0xf bound_ctrl:1
	s_nop 1
	v_add_u32_dpp v242, v242, v242 row_shr:2 row_mask:0xf bank_mask:0xf bound_ctrl:1
	s_nop 1
	v_add_u32_dpp v242, v242, v242 row_shr:4 row_mask:0xf bank_mask:0xf bound_ctrl:1
	s_nop 1
	v_add_u32_dpp v242, v242, v242 row_shr:8 row_mask:0xf bank_mask:0xf bound_ctrl:1
	s_nop 1
	v_add_u32_dpp v242, v242, v242 row_bcast:15 row_mask:0xa bank_mask:0xf
	s_nop 1
	v_add_u32_dpp v242, v242, v242 row_bcast:31 row_mask:0xc bank_mask:0xf
	s_nop 1
	v_readlane_b32 s20, v242, 63
	s_nop 1
	v_sub_u32_e32 v243, s20, v242
	v_and_b32_e32 v244, 0xffff, v243
	v_lshrrev_b32_e32 v246, 16, v243
	v_cmp_gt_u32_e64 s[58:59], s9, v244
	v_add_u32_e32 v245, v244, v240
	v_cmp_le_u32_e64 s[60:61], s9, v245
	s_and_b64 s[58:59], s[58:59], s[60:61]
	s_ff1_i32_b64 s21, s[58:59]
	s_and_b32 s21, s21, 63
	v_readlane_b32 s22, v244, s21
	v_readlane_b32 s23, v235, s21
	v_readlane_b32 s25, v234, s21
	v_readlane_b32 s26, v233, s21
	v_readlane_b32 s27, v232, s21
	s_add_u32 s28, s22, s23
	s_add_u32 s29, s28, s25
	s_add_u32 s32, s29, s26
	s_mov_b32 s37, 0
	s_mov_b32 s43, s27
	s_mov_b32 s85, s32
	s_cmp_le_u32 s9, s32
	s_cselect_b32 s37, 1, s37
	s_cselect_b32 s43, s26, s43
	s_cselect_b32 s85, s29, s85
	s_cmp_le_u32 s9, s29
	s_cselect_b32 s37, 2, s37
	s_cselect_b32 s43, s25, s43
	s_cselect_b32 s85, s28, s85
	s_cmp_le_u32 s9, s28
	s_cselect_b32 s37, 3, s37
	s_cselect_b32 s43, s23, s43
	s_cselect_b32 s85, s22, s85
	s_lshl_b32 s21, s21, 2
	s_add_i32 s21, s21, s37
	s_lshl_b32 s21, s21, s11
	s_or_b32 s21, s21, s7
	s_sub_i32 s22, s9, s85
	s_cmp_eq_u32 s43, s22
	s_cselect_b32 s23, 1, 0
	s_cmp_lg_u32 s12, 0
	s_cselect_b32 s7, s7, s21
	s_cselect_b32 s9, s9, s22
	s_cselect_b32 s12, 1, s23
	v_cmp_gt_u32_e64 s[58:59], s10, v246
	v_add_u32_e32 v245, v246, v241
	v_cmp_le_u32_e64 s[60:61], s10, v245
	s_and_b64 s[58:59], s[58:59], s[60:61]
	s_ff1_i32_b64 s21, s[58:59]
	s_and_b32 s21, s21, 63
	v_readlane_b32 s22, v246, s21
	v_readlane_b32 s23, v239, s21
	v_readlane_b32 s25, v238, s21
	v_readlane_b32 s26, v237, s21
	v_readlane_b32 s27, v236, s21
	s_add_u32 s28, s22, s23
	s_add_u32 s29, s28, s25
	s_add_u32 s32, s29, s26
	s_mov_b32 s37, 0
	s_mov_b32 s43, s27
	s_mov_b32 s85, s32
	s_cmp_le_u32 s10, s32
	s_cselect_b32 s37, 1, s37
	s_cselect_b32 s43, s26, s43
	s_cselect_b32 s85, s29, s85
	s_cmp_le_u32 s10, s29
	s_cselect_b32 s37, 2, s37
	s_cselect_b32 s43, s25, s43
	s_cselect_b32 s85, s28, s85
	s_cmp_le_u32 s10, s28
	s_cselect_b32 s37, 3, s37
	s_cselect_b32 s43, s23, s43
	s_cselect_b32 s85, s22, s85
	s_lshl_b32 s21, s21, 2
	s_add_i32 s21, s21, s37
	s_lshl_b32 s21, s21, s11
	s_or_b32 s21, s21, s8
	s_sub_i32 s22, s10, s85
	s_cmp_eq_u32 s43, s22
	s_cselect_b32 s23, 1, 0
	s_cmp_lg_u32 s13, 0
	s_cselect_b32 s8, s8, s21
	s_cselect_b32 s10, s10, s22
	s_cselect_b32 s13, 1, s23
	s_movk_i32 s11, 16
.Lsel_pass_12:
	s_and_b32 s20, s12, s13
	s_cmp_lg_u32 s20, 0
	s_cbranch_scc1 .Lsel_final_11
	ds_write_b128 v195, v[248:251]
	ds_write_b128 v195, v[248:251] offset:1280
	s_cmp_lg_u32 s12, 0
	s_cbranch_scc1 .Lsel_skip_ha_13
	v_xor_b32_e32 v9, s7, v200
	v_lshrrev_b32_e32 v9, s11, v9
	v_min_u32_e32 v9, v247, v9
	v_lshl_add_u32 v9, v9, 2, s5
	ds_add_u32 v9, v199
	v_xor_b32_e32 v10, s7, v201
	v_lshrrev_b32_e32 v10, s11, v10
	v_min_u32_e32 v10, v247, v10
	v_lshl_add_u32 v10, v10, 2, s5
	ds_add_u32 v10, v199
	v_xor_b32_e32 v11, s7, v202
	v_lshrrev_b32_e32 v11, s11, v11
	v_min_u32_e32 v11, v247, v11
	v_lshl_add_u32 v11, v11, 2, s5
	ds_add_u32 v11, v199
	v_xor_b32_e32 v12, s7, v203
	v_lshrrev_b32_e32 v12, s11, v12
	v_min_u32_e32 v12, v247, v12
	v_lshl_add_u32 v12, v12, 2, s5
	ds_add_u32 v12, v199
	v_xor_b32_e32 v9, s7, v204
	v_lshrrev_b32_e32 v9, s11, v9
	v_min_u32_e32 v9, v247, v9
	v_lshl_add_u32 v9, v9, 2, s5
	ds_add_u32 v9, v199
	v_xor_b32_e32 v10, s7, v205
	v_lshrrev_b32_e32 v10, s11, v10
	v_min_u32_e32 v10, v247, v10
	v_lshl_add_u32 v10, v10, 2, s5
	ds_add_u32 v10, v199
	v_xor_b32_e32 v11, s7, v206
	v_lshrrev_b32_e32 v11, s11, v11
	v_min_u32_e32 v11, v247, v11
	v_lshl_add_u32 v11, v11, 2, s5
	ds_add_u32 v11, v199
	v_xor_b32_e32 v12, s7, v207
	v_lshrrev_b32_e32 v12, s11, v12
	v_min_u32_e32 v12, v247, v12
	v_lshl_add_u32 v12, v12, 2, s5
	ds_add_u32 v12, v199
	s_cmp_lt_u32 s3, 8
	s_cbranch_scc1 .Lsel_pna_done_14
	v_xor_b32_e32 v9, s7, v208
	v_lshrrev_b32_e32 v9, s11, v9
	v_min_u32_e32 v9, v247, v9
	v_lshl_add_u32 v9, v9, 2, s5
	ds_add_u32 v9, v199
	v_xor_b32_e32 v10, s7, v209
	v_lshrrev_b32_e32 v10, s11, v10
	v_min_u32_e32 v10, v247, v10
	v_lshl_add_u32 v10, v10, 2, s5
	ds_add_u32 v10, v199
	v_xor_b32_e32 v11, s7, v210
	v_lshrrev_b32_e32 v11, s11, v11
	v_min_u32_e32 v11, v247, v11
	v_lshl_add_u32 v11, v11, 2, s5
	ds_add_u32 v11, v199
	v_xor_b32_e32 v12, s7, v211
	v_lshrrev_b32_e32 v12, s11, v12
	v_min_u32_e32 v12, v247, v12
	v_lshl_add_u32 v12, v12, 2, s5
	ds_add_u32 v12, v199
	s_cmp_lt_u32 s3, 12
	s_cbranch_scc1 .Lsel_pna_done_14
	v_xor_b32_e32 v9, s7, v212
	v_lshrrev_b32_e32 v9, s11, v9
	v_min_u32_e32 v9, v247, v9
	v_lshl_add_u32 v9, v9, 2, s5
	ds_add_u32 v9, v199
	v_xor_b32_e32 v10, s7, v213
	v_lshrrev_b32_e32 v10, s11, v10
	v_min_u32_e32 v10, v247, v10
	v_lshl_add_u32 v10, v10, 2, s5
	ds_add_u32 v10, v199
	v_xor_b32_e32 v11, s7, v214
	v_lshrrev_b32_e32 v11, s11, v11
	v_min_u32_e32 v11, v247, v11
	v_lshl_add_u32 v11, v11, 2, s5
	ds_add_u32 v11, v199
	v_xor_b32_e32 v12, s7, v215
	v_lshrrev_b32_e32 v12, s11, v12
	v_min_u32_e32 v12, v247, v12
	v_lshl_add_u32 v12, v12, 2, s5
	ds_add_u32 v12, v199
	s_cmp_lt_u32 s3, 16
	s_cbranch_scc1 .Lsel_pna_done_14
	v_xor_b32_e32 v9, s7, v216
	v_lshrrev_b32_e32 v9, s11, v9
	v_min_u32_e32 v9, v247, v9
	v_lshl_add_u32 v9, v9, 2, s5
	ds_add_u32 v9, v199
	v_xor_b32_e32 v10, s7, v217
	v_lshrrev_b32_e32 v10, s11, v10
	v_min_u32_e32 v10, v247, v10
	v_lshl_add_u32 v10, v10, 2, s5
	ds_add_u32 v10, v199
	v_xor_b32_e32 v11, s7, v218
	v_lshrrev_b32_e32 v11, s11, v11
	v_min_u32_e32 v11, v247, v11
	v_lshl_add_u32 v11, v11, 2, s5
	ds_add_u32 v11, v199
	v_xor_b32_e32 v12, s7, v219
	v_lshrrev_b32_e32 v12, s11, v12
	v_min_u32_e32 v12, v247, v12
	v_lshl_add_u32 v12, v12, 2, s5
	ds_add_u32 v12, v199
	s_cmp_lt_u32 s3, 20
	s_cbranch_scc1 .Lsel_pna_done_14
	v_xor_b32_e32 v9, s7, v220
	v_lshrrev_b32_e32 v9, s11, v9
	v_min_u32_e32 v9, v247, v9
	v_lshl_add_u32 v9, v9, 2, s5
	ds_add_u32 v9, v199
	v_xor_b32_e32 v10, s7, v221
	v_lshrrev_b32_e32 v10, s11, v10
	v_min_u32_e32 v10, v247, v10
	v_lshl_add_u32 v10, v10, 2, s5
	ds_add_u32 v10, v199
	v_xor_b32_e32 v11, s7, v222
	v_lshrrev_b32_e32 v11, s11, v11
	v_min_u32_e32 v11, v247, v11
	v_lshl_add_u32 v11, v11, 2, s5
	ds_add_u32 v11, v199
	v_xor_b32_e32 v12, s7, v223
	v_lshrrev_b32_e32 v12, s11, v12
	v_min_u32_e32 v12, v247, v12
	v_lshl_add_u32 v12, v12, 2, s5
	ds_add_u32 v12, v199
	s_cmp_lt_u32 s3, 24
	s_cbranch_scc1 .Lsel_pna_done_14
	v_xor_b32_e32 v9, s7, v224
	v_lshrrev_b32_e32 v9, s11, v9
	v_min_u32_e32 v9, v247, v9
	v_lshl_add_u32 v9, v9, 2, s5
	ds_add_u32 v9, v199
	v_xor_b32_e32 v10, s7, v225
	v_lshrrev_b32_e32 v10, s11, v10
	v_min_u32_e32 v10, v247, v10
	v_lshl_add_u32 v10, v10, 2, s5
	ds_add_u32 v10, v199
	v_xor_b32_e32 v11, s7, v226
	v_lshrrev_b32_e32 v11, s11, v11
	v_min_u32_e32 v11, v247, v11
	v_lshl_add_u32 v11, v11, 2, s5
	ds_add_u32 v11, v199
	v_xor_b32_e32 v12, s7, v227
	v_lshrrev_b32_e32 v12, s11, v12
	v_min_u32_e32 v12, v247, v12
	v_lshl_add_u32 v12, v12, 2, s5
	ds_add_u32 v12, v199
	s_cmp_lt_u32 s3, 28
	s_cbranch_scc1 .Lsel_pna_done_14
	v_xor_b32_e32 v9, s7, v228
	v_lshrrev_b32_e32 v9, s11, v9
	v_min_u32_e32 v9, v247, v9
	v_lshl_add_u32 v9, v9, 2, s5
	ds_add_u32 v9, v199
	v_xor_b32_e32 v10, s7, v229
	v_lshrrev_b32_e32 v10, s11, v10
	v_min_u32_e32 v10, v247, v10
	v_lshl_add_u32 v10, v10, 2, s5
	ds_add_u32 v10, v199
	v_xor_b32_e32 v11, s7, v230
	v_lshrrev_b32_e32 v11, s11, v11
	v_min_u32_e32 v11, v247, v11
	v_lshl_add_u32 v11, v11, 2, s5
	ds_add_u32 v11, v199
	v_xor_b32_e32 v12, s7, v231
	v_lshrrev_b32_e32 v12, s11, v12
	v_min_u32_e32 v12, v247, v12
	v_lshl_add_u32 v12, v12, 2, s5
	ds_add_u32 v12, v199
.Lsel_pna_done_14:
.Lsel_skip_ha_13:
	s_cmp_lg_u32 s13, 0
	s_cbranch_scc1 .Lsel_skip_hb_15
	v_xor_b32_e32 v9, s8, v148
	v_lshrrev_b32_e32 v9, s11, v9
	v_min_u32_e32 v9, v247, v9
	v_lshl_add_u32 v9, v9, 2, s6
	ds_add_u32 v9, v199
	v_xor_b32_e32 v10, s8, v149
	v_lshrrev_b32_e32 v10, s11, v10
	v_min_u32_e32 v10, v247, v10
	v_lshl_add_u32 v10, v10, 2, s6
	ds_add_u32 v10, v199
	v_xor_b32_e32 v11, s8, v150
	v_lshrrev_b32_e32 v11, s11, v11
	v_min_u32_e32 v11, v247, v11
	v_lshl_add_u32 v11, v11, 2, s6
	ds_add_u32 v11, v199
	v_xor_b32_e32 v12, s8, v151
	v_lshrrev_b32_e32 v12, s11, v12
	v_min_u32_e32 v12, v247, v12
	v_lshl_add_u32 v12, v12, 2, s6
	ds_add_u32 v12, v199
	v_xor_b32_e32 v9, s8, v152
	v_lshrrev_b32_e32 v9, s11, v9
	v_min_u32_e32 v9, v247, v9
	v_lshl_add_u32 v9, v9, 2, s6
	ds_add_u32 v9, v199
	v_xor_b32_e32 v10, s8, v153
	v_lshrrev_b32_e32 v10, s11, v10
	v_min_u32_e32 v10, v247, v10
	v_lshl_add_u32 v10, v10, 2, s6
	ds_add_u32 v10, v199
	v_xor_b32_e32 v11, s8, v154
	v_lshrrev_b32_e32 v11, s11, v11
	v_min_u32_e32 v11, v247, v11
	v_lshl_add_u32 v11, v11, 2, s6
	ds_add_u32 v11, v199
	v_xor_b32_e32 v12, s8, v155
	v_lshrrev_b32_e32 v12, s11, v12
	v_min_u32_e32 v12, v247, v12
	v_lshl_add_u32 v12, v12, 2, s6
	ds_add_u32 v12, v199
	s_cmp_lt_u32 s3, 8
	s_cbranch_scc1 .Lsel_pnb_done_16
	v_xor_b32_e32 v9, s8, v156
	v_lshrrev_b32_e32 v9, s11, v9
	v_min_u32_e32 v9, v247, v9
	v_lshl_add_u32 v9, v9, 2, s6
	ds_add_u32 v9, v199
	v_xor_b32_e32 v10, s8, v157
	v_lshrrev_b32_e32 v10, s11, v10
	v_min_u32_e32 v10, v247, v10
	v_lshl_add_u32 v10, v10, 2, s6
	ds_add_u32 v10, v199
	v_xor_b32_e32 v11, s8, v158
	v_lshrrev_b32_e32 v11, s11, v11
	v_min_u32_e32 v11, v247, v11
	v_lshl_add_u32 v11, v11, 2, s6
	ds_add_u32 v11, v199
	v_xor_b32_e32 v12, s8, v159
	v_lshrrev_b32_e32 v12, s11, v12
	v_min_u32_e32 v12, v247, v12
	v_lshl_add_u32 v12, v12, 2, s6
	ds_add_u32 v12, v199
	s_cmp_lt_u32 s3, 12
	s_cbranch_scc1 .Lsel_pnb_done_16
	v_xor_b32_e32 v9, s8, v160
	v_lshrrev_b32_e32 v9, s11, v9
	v_min_u32_e32 v9, v247, v9
	v_lshl_add_u32 v9, v9, 2, s6
	ds_add_u32 v9, v199
	v_xor_b32_e32 v10, s8, v161
	v_lshrrev_b32_e32 v10, s11, v10
	v_min_u32_e32 v10, v247, v10
	v_lshl_add_u32 v10, v10, 2, s6
	ds_add_u32 v10, v199
	v_xor_b32_e32 v11, s8, v162
	v_lshrrev_b32_e32 v11, s11, v11
	v_min_u32_e32 v11, v247, v11
	v_lshl_add_u32 v11, v11, 2, s6
	ds_add_u32 v11, v199
	v_xor_b32_e32 v12, s8, v163
	v_lshrrev_b32_e32 v12, s11, v12
	v_min_u32_e32 v12, v247, v12
	v_lshl_add_u32 v12, v12, 2, s6
	ds_add_u32 v12, v199
	s_cmp_lt_u32 s3, 16
	s_cbranch_scc1 .Lsel_pnb_done_16
	v_xor_b32_e32 v9, s8, v164
	v_lshrrev_b32_e32 v9, s11, v9
	v_min_u32_e32 v9, v247, v9
	v_lshl_add_u32 v9, v9, 2, s6
	ds_add_u32 v9, v199
	v_xor_b32_e32 v10, s8, v165
	v_lshrrev_b32_e32 v10, s11, v10
	v_min_u32_e32 v10, v247, v10
	v_lshl_add_u32 v10, v10, 2, s6
	ds_add_u32 v10, v199
	v_xor_b32_e32 v11, s8, v166
	v_lshrrev_b32_e32 v11, s11, v11
	v_min_u32_e32 v11, v247, v11
	v_lshl_add_u32 v11, v11, 2, s6
	ds_add_u32 v11, v199
	v_xor_b32_e32 v12, s8, v167
	v_lshrrev_b32_e32 v12, s11, v12
	v_min_u32_e32 v12, v247, v12
	v_lshl_add_u32 v12, v12, 2, s6
	ds_add_u32 v12, v199
	s_cmp_lt_u32 s3, 20
	s_cbranch_scc1 .Lsel_pnb_done_16
	v_xor_b32_e32 v9, s8, v168
	v_lshrrev_b32_e32 v9, s11, v9
	v_min_u32_e32 v9, v247, v9
	v_lshl_add_u32 v9, v9, 2, s6
	ds_add_u32 v9, v199
	v_xor_b32_e32 v10, s8, v169
	v_lshrrev_b32_e32 v10, s11, v10
	v_min_u32_e32 v10, v247, v10
	v_lshl_add_u32 v10, v10, 2, s6
	ds_add_u32 v10, v199
	v_xor_b32_e32 v11, s8, v170
	v_lshrrev_b32_e32 v11, s11, v11
	v_min_u32_e32 v11, v247, v11
	v_lshl_add_u32 v11, v11, 2, s6
	ds_add_u32 v11, v199
	v_xor_b32_e32 v12, s8, v171
	v_lshrrev_b32_e32 v12, s11, v12
	v_min_u32_e32 v12, v247, v12
	v_lshl_add_u32 v12, v12, 2, s6
	ds_add_u32 v12, v199
	s_cmp_lt_u32 s3, 24
	s_cbranch_scc1 .Lsel_pnb_done_16
	v_xor_b32_e32 v9, s8, v172
	v_lshrrev_b32_e32 v9, s11, v9
	v_min_u32_e32 v9, v247, v9
	v_lshl_add_u32 v9, v9, 2, s6
	ds_add_u32 v9, v199
	v_xor_b32_e32 v10, s8, v173
	v_lshrrev_b32_e32 v10, s11, v10
	v_min_u32_e32 v10, v247, v10
	v_lshl_add_u32 v10, v10, 2, s6
	ds_add_u32 v10, v199
	v_xor_b32_e32 v11, s8, v174
	v_lshrrev_b32_e32 v11, s11, v11
	v_min_u32_e32 v11, v247, v11
	v_lshl_add_u32 v11, v11, 2, s6
	ds_add_u32 v11, v199
	v_xor_b32_e32 v12, s8, v175
	v_lshrrev_b32_e32 v12, s11, v12
	v_min_u32_e32 v12, v247, v12
	v_lshl_add_u32 v12, v12, 2, s6
	ds_add_u32 v12, v199
	s_cmp_lt_u32 s3, 28
	s_cbranch_scc1 .Lsel_pnb_done_16
	v_xor_b32_e32 v9, s8, v176
	v_lshrrev_b32_e32 v9, s11, v9
	v_min_u32_e32 v9, v247, v9
	v_lshl_add_u32 v9, v9, 2, s6
	ds_add_u32 v9, v199
	v_xor_b32_e32 v10, s8, v177
	v_lshrrev_b32_e32 v10, s11, v10
	v_min_u32_e32 v10, v247, v10
	v_lshl_add_u32 v10, v10, 2, s6
	ds_add_u32 v10, v199
	v_xor_b32_e32 v11, s8, v186
	v_lshrrev_b32_e32 v11, s11, v11
	v_min_u32_e32 v11, v247, v11
	v_lshl_add_u32 v11, v11, 2, s6
	ds_add_u32 v11, v199
	v_xor_b32_e32 v12, s8, v187
	v_lshrrev_b32_e32 v12, s11, v12
	v_min_u32_e32 v12, v247, v12
	v_lshl_add_u32 v12, v12, 2, s6
	ds_add_u32 v12, v199
.Lsel_pnb_done_16:
.Lsel_skip_hb_15:
	s_waitcnt lgkmcnt(0)
	ds_read_b128 v[232:235], v195
	ds_read_b128 v[236:239], v195 offset:1280
	s_waitcnt lgkmcnt(0)
	v_add3_u32 v240, v232, v233, v234
	v_add3_u32 v241, v236, v237, v238
	v_add_u32_e32 v240, v240, v235
	v_add_u32_e32 v241, v241, v239
	v_lshl_add_u32 v242, v241, 16, v240
	s_nop 1
	v_add_u32_dpp v242, v242, v242 row_shr:1 row_mask:0xf bank_mask:0xf bound_ctrl:1
	s_nop 1
	v_add_u32_dpp v242, v242, v242 row_shr:2 row_mask:0xf bank_mask:0xf bound_ctrl:1
	s_nop 1
	v_add_u32_dpp v242, v242, v242 row_shr:4 row_mask:0xf bank_mask:0xf bound_ctrl:1
	s_nop 1
	v_add_u32_dpp v242, v242, v242 row_shr:8 row_mask:0xf bank_mask:0xf bound_ctrl:1
	s_nop 1
	v_add_u32_dpp v242, v242, v242 row_bcast:15 row_mask:0xa bank_mask:0xf
	s_nop 1
	v_add_u32_dpp v242, v242, v242 row_bcast:31 row_mask:0xc bank_mask:0xf
	s_nop 1
	v_readlane_b32 s20, v242, 63
	s_nop 1
	v_sub_u32_e32 v243, s20, v242
	v_and_b32_e32 v244, 0xffff, v243
	v_lshrrev_b32_e32 v246, 16, v243
	v_cmp_gt_u32_e64 s[58:59], s9, v244
	v_add_u32_e32 v245, v244, v240
	v_cmp_le_u32_e64 s[60:61], s9, v245
	s_and_b64 s[58:59], s[58:59], s[60:61]
	s_ff1_i32_b64 s21, s[58:59]
	s_and_b32 s21, s21, 63
	v_readlane_b32 s22, v244, s21
	v_readlane_b32 s23, v235, s21
	v_readlane_b32 s25, v234, s21
	v_readlane_b32 s26, v233, s21
	v_readlane_b32 s27, v232, s21
	s_add_u32 s28, s22, s23
	s_add_u32 s29, s28, s25
	s_add_u32 s32, s29, s26
	s_mov_b32 s37, 0
	s_mov_b32 s43, s27
	s_mov_b32 s85, s32
	s_cmp_le_u32 s9, s32
	s_cselect_b32 s37, 1, s37
	s_cselect_b32 s43, s26, s43
	s_cselect_b32 s85, s29, s85
	s_cmp_le_u32 s9, s29
	s_cselect_b32 s37, 2, s37
	s_cselect_b32 s43, s25, s43
	s_cselect_b32 s85, s28, s85
	s_cmp_le_u32 s9, s28
	s_cselect_b32 s37, 3, s37
	s_cselect_b32 s43, s23, s43
	s_cselect_b32 s85, s22, s85
	s_lshl_b32 s21, s21, 2
	s_add_i32 s21, s21, s37
	s_lshl_b32 s21, s21, s11
	s_or_b32 s21, s21, s7
	s_sub_i32 s22, s9, s85
	s_cmp_eq_u32 s43, s22
	s_cselect_b32 s23, 1, 0
	s_cmp_lg_u32 s12, 0
	s_cselect_b32 s7, s7, s21
	s_cselect_b32 s9, s9, s22
	s_cselect_b32 s12, 1, s23
	v_cmp_gt_u32_e64 s[58:59], s10, v246
	v_add_u32_e32 v245, v246, v241
	v_cmp_le_u32_e64 s[60:61], s10, v245
	s_and_b64 s[58:59], s[58:59], s[60:61]
	s_ff1_i32_b64 s21, s[58:59]
	s_and_b32 s21, s21, 63
	v_readlane_b32 s22, v246, s21
	v_readlane_b32 s23, v239, s21
	v_readlane_b32 s25, v238, s21
	v_readlane_b32 s26, v237, s21
	v_readlane_b32 s27, v236, s21
	s_add_u32 s28, s22, s23
	s_add_u32 s29, s28, s25
	s_add_u32 s32, s29, s26
	s_mov_b32 s37, 0
	s_mov_b32 s43, s27
	s_mov_b32 s85, s32
	s_cmp_le_u32 s10, s32
	s_cselect_b32 s37, 1, s37
	s_cselect_b32 s43, s26, s43
	s_cselect_b32 s85, s29, s85
	s_cmp_le_u32 s10, s29
	s_cselect_b32 s37, 2, s37
	s_cselect_b32 s43, s25, s43
	s_cselect_b32 s85, s28, s85
	s_cmp_le_u32 s10, s28
	s_cselect_b32 s37, 3, s37
	s_cselect_b32 s43, s23, s43
	s_cselect_b32 s85, s22, s85
	s_lshl_b32 s21, s21, 2
	s_add_i32 s21, s21, s37
	s_lshl_b32 s21, s21, s11
	s_or_b32 s21, s21, s8
	s_sub_i32 s22, s10, s85
	s_cmp_eq_u32 s43, s22
	s_cselect_b32 s23, 1, 0
	s_cmp_lg_u32 s13, 0
	s_cselect_b32 s8, s8, s21
	s_cselect_b32 s10, s10, s22
	s_cselect_b32 s13, 1, s23
	s_sub_i32 s11, s11, 8
	s_cmp_ge_i32 s11, 0
	s_cbranch_scc1 .Lsel_pass_12
.Lsel_final_11:
	s_cmp_lg_u32 s12, 0
	s_cbranch_scc0 .Lsel_tiea_17
	v_cmp_le_u32_e64 s[58:59], s7, v200
	v_cmp_le_u32_e64 s[60:61], s7, v201
	v_cmp_le_u32_e64 s[62:63], s7, v202
	v_cmp_le_u32_e64 s[68:69], s7, v203
	v_writelane_b32 v2, s58, 0
	v_writelane_b32 v3, s59, 0
	v_writelane_b32 v2, s60, 1
	v_writelane_b32 v3, s61, 1
	v_writelane_b32 v2, s62, 2
	v_writelane_b32 v3, s63, 2
	v_writelane_b32 v2, s68, 3
	v_writelane_b32 v3, s69, 3
	v_cmp_le_u32_e64 s[58:59], s7, v204
	v_cmp_le_u32_e64 s[60:61], s7, v205
	v_cmp_le_u32_e64 s[62:63], s7, v206
	v_cmp_le_u32_e64 s[68:69], s7, v207
	v_writelane_b32 v2, s58, 4
	v_writelane_b32 v3, s59, 4
	v_writelane_b32 v2, s60, 5
	v_writelane_b32 v3, s61, 5
	v_writelane_b32 v2, s62, 6
	v_writelane_b32 v3, s63, 6
	v_writelane_b32 v2, s68, 7
	v_writelane_b32 v3, s69, 7
	s_cmp_lt_u32 s3, 8
	s_cbranch_scc1 .Lsel_fea_done_19
	v_cmp_le_u32_e64 s[58:59], s7, v208
	v_cmp_le_u32_e64 s[60:61], s7, v209
	v_cmp_le_u32_e64 s[62:63], s7, v210
	v_cmp_le_u32_e64 s[68:69], s7, v211
	v_writelane_b32 v2, s58, 8
	v_writelane_b32 v3, s59, 8
	v_writelane_b32 v2, s60, 9
	v_writelane_b32 v3, s61, 9
	v_writelane_b32 v2, s62, 10
	v_writelane_b32 v3, s63, 10
	v_writelane_b32 v2, s68, 11
	v_writelane_b32 v3, s69, 11
	s_cmp_lt_u32 s3, 12
	s_cbranch_scc1 .Lsel_fea_done_19
	v_cmp_le_u32_e64 s[58:59], s7, v212
	v_cmp_le_u32_e64 s[60:61], s7, v213
	v_cmp_le_u32_e64 s[62:63], s7, v214
	v_cmp_le_u32_e64 s[68:69], s7, v215
	v_writelane_b32 v2, s58, 12
	v_writelane_b32 v3, s59, 12
	v_writelane_b32 v2, s60, 13
	v_writelane_b32 v3, s61, 13
	v_writelane_b32 v2, s62, 14
	v_writelane_b32 v3, s63, 14
	v_writelane_b32 v2, s68, 15
	v_writelane_b32 v3, s69, 15
	s_cmp_lt_u32 s3, 16
	s_cbranch_scc1 .Lsel_fea_done_19
	v_cmp_le_u32_e64 s[58:59], s7, v216
	v_cmp_le_u32_e64 s[60:61], s7, v217
	v_cmp_le_u32_e64 s[62:63], s7, v218
	v_cmp_le_u32_e64 s[68:69], s7, v219
	v_writelane_b32 v2, s58, 16
	v_writelane_b32 v3, s59, 16
	v_writelane_b32 v2, s60, 17
	v_writelane_b32 v3, s61, 17
	v_writelane_b32 v2, s62, 18
	v_writelane_b32 v3, s63, 18
	v_writelane_b32 v2, s68, 19
	v_writelane_b32 v3, s69, 19
	s_cmp_lt_u32 s3, 20
	s_cbranch_scc1 .Lsel_fea_done_19
	v_cmp_le_u32_e64 s[58:59], s7, v220
	v_cmp_le_u32_e64 s[60:61], s7, v221
	v_cmp_le_u32_e64 s[62:63], s7, v222
	v_cmp_le_u32_e64 s[68:69], s7, v223
	v_writelane_b32 v2, s58, 20
	v_writelane_b32 v3, s59, 20
	v_writelane_b32 v2, s60, 21
	v_writelane_b32 v3, s61, 21
	v_writelane_b32 v2, s62, 22
	v_writelane_b32 v3, s63, 22
	v_writelane_b32 v2, s68, 23
	v_writelane_b32 v3, s69, 23
	s_cmp_lt_u32 s3, 24
	s_cbranch_scc1 .Lsel_fea_done_19
	v_cmp_le_u32_e64 s[58:59], s7, v224
	v_cmp_le_u32_e64 s[60:61], s7, v225
	v_cmp_le_u32_e64 s[62:63], s7, v226
	v_cmp_le_u32_e64 s[68:69], s7, v227
	v_writelane_b32 v2, s58, 24
	v_writelane_b32 v3, s59, 24
	v_writelane_b32 v2, s60, 25
	v_writelane_b32 v3, s61, 25
	v_writelane_b32 v2, s62, 26
	v_writelane_b32 v3, s63, 26
	v_writelane_b32 v2, s68, 27
	v_writelane_b32 v3, s69, 27
	s_cmp_lt_u32 s3, 28
	s_cbranch_scc1 .Lsel_fea_done_19
	v_cmp_le_u32_e64 s[58:59], s7, v228
	v_cmp_le_u32_e64 s[60:61], s7, v229
	v_cmp_le_u32_e64 s[62:63], s7, v230
	v_cmp_le_u32_e64 s[68:69], s7, v231
	v_writelane_b32 v2, s58, 28
	v_writelane_b32 v3, s59, 28
	v_writelane_b32 v2, s60, 29
	v_writelane_b32 v3, s61, 29
	v_writelane_b32 v2, s62, 30
	v_writelane_b32 v3, s63, 30
	v_writelane_b32 v2, s68, 31
	v_writelane_b32 v3, s69, 31

.Lsel_tiea_17:
	v_cmp_eq_u32_e64 s[58:59], s7, v200
	v_cmp_lt_u32_e64 s[60:61], s7, v200
	s_nop 1
	v_mbcnt_lo_u32_b32 v245, s58, 0
	v_mbcnt_hi_u32_b32 v245, s59, v245
	v_cmp_gt_i32_e64 s[62:63], s9, v245
	s_bcnt1_i32_b64 s20, s[58:59]
	s_and_b64 s[62:63], s[62:63], s[58:59]
	s_or_b64 s[62:63], s[62:63], s[60:61]
	s_sub_i32 s9, s9, s20
	v_writelane_b32 v2, s62, 0
	v_writelane_b32 v3, s63, 0
	v_cmp_eq_u32_e64 s[58:59], s7, v201
	v_cmp_lt_u32_e64 s[60:61], s7, v201
	s_nop 1
	v_mbcnt_lo_u32_b32 v245, s58, 0
	v_mbcnt_hi_u32_b32 v245, s59, v245
	v_cmp_gt_i32_e64 s[62:63], s9, v245
	s_bcnt1_i32_b64 s20, s[58:59]
	s_and_b64 s[62:63], s[62:63], s[58:59]
	s_or_b64 s[62:63], s[62:63], s[60:61]
	s_sub_i32 s9, s9, s20
	v_writelane_b32 v2, s62, 1
	v_writelane_b32 v3, s63, 1
	v_cmp_eq_u32_e64 s[58:59], s7, v202
	v_cmp_lt_u32_e64 s[60:61], s7, v202
	s_nop 1
	v_mbcnt_lo_u32_b32 v245, s58, 0
	v_mbcnt_hi_u32_b32 v245, s59, v245
	v_cmp_gt_i32_e64 s[62:63], s9, v245
	s_bcnt1_i32_b64 s20, s[58:59]
	s_and_b64 s[62:63], s[62:63], s[58:59]
	s_or_b64 s[62:63], s[62:63], s[60:61]
	s_sub_i32 s9, s9, s20
	v_writelane_b32 v2, s62, 2
	v_writelane_b32 v3, s63, 2
	v_cmp_eq_u32_e64 s[58:59], s7, v203
	v_cmp_lt_u32_e64 s[60:61], s7, v203
	s_nop 1
	v_mbcnt_lo_u32_b32 v245, s58, 0
	v_mbcnt_hi_u32_b32 v245, s59, v245
	v_cmp_gt_i32_e64 s[62:63], s9, v245
	s_bcnt1_i32_b64 s20, s[58:59]
	s_and_b64 s[62:63], s[62:63], s[58:59]
	s_or_b64 s[62:63], s[62:63], s[60:61]
	s_sub_i32 s9, s9, s20
	v_writelane_b32 v2, s62, 3
	v_writelane_b32 v3, s63, 3
	v_cmp_eq_u32_e64 s[58:59], s7, v204
	v_cmp_lt_u32_e64 s[60:61], s7, v204
	s_nop 1
	v_mbcnt_lo_u32_b32 v245, s58, 0
	v_mbcnt_hi_u32_b32 v245, s59, v245
	v_cmp_gt_i32_e64 s[62:63], s9, v245
	s_bcnt1_i32_b64 s20, s[58:59]
	s_and_b64 s[62:63], s[62:63], s[58:59]
	s_or_b64 s[62:63], s[62:63], s[60:61]
	s_sub_i32 s9, s9, s20
	v_writelane_b32 v2, s62, 4
	v_writelane_b32 v3, s63, 4
	v_cmp_eq_u32_e64 s[58:59], s7, v205
	v_cmp_lt_u32_e64 s[60:61], s7, v205
	s_nop 1
	v_mbcnt_lo_u32_b32 v245, s58, 0
	v_mbcnt_hi_u32_b32 v245, s59, v245
	v_cmp_gt_i32_e64 s[62:63], s9, v245
	s_bcnt1_i32_b64 s20, s[58:59]
	s_and_b64 s[62:63], s[62:63], s[58:59]
	s_or_b64 s[62:63], s[62:63], s[60:61]
	s_sub_i32 s9, s9, s20
	v_writelane_b32 v2, s62, 5
	v_writelane_b32 v3, s63, 5
	v_cmp_eq_u32_e64 s[58:59], s7, v206
	v_cmp_lt_u32_e64 s[60:61], s7, v206
	s_nop 1
	v_mbcnt_lo_u32_b32 v245, s58, 0
	v_mbcnt_hi_u32_b32 v245, s59, v245
	v_cmp_gt_i32_e64 s[62:63], s9, v245
	s_bcnt1_i32_b64 s20, s[58:59]
	s_and_b64 s[62:63], s[62:63], s[58:59]
	s_or_b64 s[62:63], s[62:63], s[60:61]
	s_sub_i32 s9, s9, s20
	v_writelane_b32 v2, s62, 6
	v_writelane_b32 v3, s63, 6
	v_cmp_eq_u32_e64 s[58:59], s7, v207
	v_cmp_lt_u32_e64 s[60:61], s7, v207
	s_nop 1
	v_mbcnt_lo_u32_b32 v245, s58, 0
	v_mbcnt_hi_u32_b32 v245, s59, v245
	v_cmp_gt_i32_e64 s[62:63], s9, v245
	s_bcnt1_i32_b64 s20, s[58:59]
	s_and_b64 s[62:63], s[62:63], s[58:59]
	s_or_b64 s[62:63], s[62:63], s[60:61]
	s_sub_i32 s9, s9, s20
	v_writelane_b32 v2, s62, 7
	v_writelane_b32 v3, s63, 7
	s_cmp_lt_u32 s3, 8
	s_cbranch_scc1 .Lsel_fta_done_20
	v_cmp_eq_u32_e64 s[58:59], s7, v208
	v_cmp_lt_u32_e64 s[60:61], s7, v208
	s_nop 1
	v_mbcnt_lo_u32_b32 v245, s58, 0
	v_mbcnt_hi_u32_b32 v245, s59, v245
	v_cmp_gt_i32_e64 s[62:63], s9, v245
	s_bcnt1_i32_b64 s20, s[58:59]
	s_and_b64 s[62:63], s[62:63], s[58:59]
	s_or_b64 s[62:63], s[62:63], s[60:61]
	s_sub_i32 s9, s9, s20
	v_writelane_b32 v2, s62, 8
	v_writelane_b32 v3, s63, 8
	v_cmp_eq_u32_e64 s[58:59], s7, v209
	v_cmp_lt_u32_e64 s[60:61], s7, v209
	s_nop 1
	v_mbcnt_lo_u32_b32 v245, s58, 0
	v_mbcnt_hi_u32_b32 v245, s59, v245
	v_cmp_gt_i32_e64 s[62:63], s9, v245
	s_bcnt1_i32_b64 s20, s[58:59]
	s_and_b64 s[62:63], s[62:63], s[58:59]
	s_or_b64 s[62:63], s[62:63], s[60:61]
	s_sub_i32 s9, s9, s20
	v_writelane_b32 v2, s62, 9
	v_writelane_b32 v3, s63, 9
	v_cmp_eq_u32_e64 s[58:59], s7, v210
	v_cmp_lt_u32_e64 s[60:61], s7, v210
	s_nop 1
	v_mbcnt_lo_u32_b32 v245, s58, 0
	v_mbcnt_hi_u32_b32 v245, s59, v245
	v_cmp_gt_i32_e64 s[62:63], s9, v245
	s_bcnt1_i32_b64 s20, s[58:59]
	s_and_b64 s[62:63], s[62:63], s[58:59]
	s_or_b64 s[62:63], s[62:63], s[60:61]
	s_sub_i32 s9, s9, s20
	v_writelane_b32 v2, s62, 10
	v_writelane_b32 v3, s63, 10
	v_cmp_eq_u32_e64 s[58:59], s7, v211
	v_cmp_lt_u32_e64 s[60:61], s7, v211
	s_nop 1
	v_mbcnt_lo_u32_b32 v245, s58, 0
	v_mbcnt_hi_u32_b32 v245, s59, v245
	v_cmp_gt_i32_e64 s[62:63], s9, v245
	s_bcnt1_i32_b64 s20, s[58:59]
	s_and_b64 s[62:63], s[62:63], s[58:59]
	s_or_b64 s[62:63], s[62:63], s[60:61]
	s_sub_i32 s9, s9, s20
	v_writelane_b32 v2, s62, 11
	v_writelane_b32 v3, s63, 11
	s_cmp_lt_u32 s3, 12
	s_cbranch_scc1 .Lsel_fta_done_20
	v_cmp_eq_u32_e64 s[58:59], s7, v212
	v_cmp_lt_u32_e64 s[60:61], s7, v212
	s_nop 1
	v_mbcnt_lo_u32_b32 v245, s58, 0
	v_mbcnt_hi_u32_b32 v245, s59, v245
	v_cmp_gt_i32_e64 s[62:63], s9, v245
	s_bcnt1_i32_b64 s20, s[58:59]
	s_and_b64 s[62:63], s[62:63], s[58:59]
	s_or_b64 s[62:63], s[62:63], s[60:61]
	s_sub_i32 s9, s9, s20
	v_writelane_b32 v2, s62, 12
	v_writelane_b32 v3, s63, 12
	v_cmp_eq_u32_e64 s[58:59], s7, v213
	v_cmp_lt_u32_e64 s[60:61], s7, v213
	s_nop 1
	v_mbcnt_lo_u32_b32 v245, s58, 0
	v_mbcnt_hi_u32_b32 v245, s59, v245
	v_cmp_gt_i32_e64 s[62:63], s9, v245
	s_bcnt1_i32_b64 s20, s[58:59]
	s_and_b64 s[62:63], s[62:63], s[58:59]
	s_or_b64 s[62:63], s[62:63], s[60:61]
	s_sub_i32 s9, s9, s20
	v_writelane_b32 v2, s62, 13
	v_writelane_b32 v3, s63, 13
	v_cmp_eq_u32_e64 s[58:59], s7, v214
	v_cmp_lt_u32_e64 s[60:61], s7, v214
	s_nop 1
	v_mbcnt_lo_u32_b32 v245, s58, 0
	v_mbcnt_hi_u32_b32 v245, s59, v245
	v_cmp_gt_i32_e64 s[62:63], s9, v245
	s_bcnt1_i32_b64 s20, s[58:59]
	s_and_b64 s[62:63], s[62:63], s[58:59]
	s_or_b64 s[62:63], s[62:63], s[60:61]
	s_sub_i32 s9, s9, s20
	v_writelane_b32 v2, s62, 14
	v_writelane_b32 v3, s63, 14
	v_cmp_eq_u32_e64 s[58:59], s7, v215
	v_cmp_lt_u32_e64 s[60:61], s7, v215
	s_nop 1
	v_mbcnt_lo_u32_b32 v245, s58, 0
	v_mbcnt_hi_u32_b32 v245, s59, v245
	v_cmp_gt_i32_e64 s[62:63], s9, v245
	s_bcnt1_i32_b64 s20, s[58:59]
	s_and_b64 s[62:63], s[62:63], s[58:59]
	s_or_b64 s[62:63], s[62:63], s[60:61]
	s_sub_i32 s9, s9, s20
	v_writelane_b32 v2, s62, 15
	v_writelane_b32 v3, s63, 15
	s_cmp_lt_u32 s3, 16
	s_cbranch_scc1 .Lsel_fta_done_20
	v_cmp_eq_u32_e64 s[58:59], s7, v216
	v_cmp_lt_u32_e64 s[60:61], s7, v216
	s_nop 1
	v_mbcnt_lo_u32_b32 v245, s58, 0
	v_mbcnt_hi_u32_b32 v245, s59, v245
	v_cmp_gt_i32_e64 s[62:63], s9, v245
	s_bcnt1_i32_b64 s20, s[58:59]
	s_and_b64 s[62:63], s[62:63], s[58:59]
	s_or_b64 s[62:63], s[62:63], s[60:61]
	s_sub_i32 s9, s9, s20
	v_writelane_b32 v2, s62, 16
	v_writelane_b32 v3, s63, 16
	v_cmp_eq_u32_e64 s[58:59], s7, v217
	v_cmp_lt_u32_e64 s[60:61], s7, v217
	s_nop 1
	v_mbcnt_lo_u32_b32 v245, s58, 0
	v_mbcnt_hi_u32_b32 v245, s59, v245
	v_cmp_gt_i32_e64 s[62:63], s9, v245
	s_bcnt1_i32_b64 s20, s[58:59]
	s_and_b64 s[62:63], s[62:63], s[58:59]
	s_or_b64 s[62:63], s[62:63], s[60:61]
	s_sub_i32 s9, s9, s20
	v_writelane_b32 v2, s62, 17
	v_writelane_b32 v3, s63, 17
	v_cmp_eq_u32_e64 s[58:59], s7, v218
	v_cmp_lt_u32_e64 s[60:61], s7, v218
	s_nop 1
	v_mbcnt_lo_u32_b32 v245, s58, 0
	v_mbcnt_hi_u32_b32 v245, s59, v245
	v_cmp_gt_i32_e64 s[62:63], s9, v245
	s_bcnt1_i32_b64 s20, s[58:59]
	s_and_b64 s[62:63], s[62:63], s[58:59]
	s_or_b64 s[62:63], s[62:63], s[60:61]
	s_sub_i32 s9, s9, s20
	v_writelane_b32 v2, s62, 18
	v_writelane_b32 v3, s63, 18
	v_cmp_eq_u32_e64 s[58:59], s7, v219
	v_cmp_lt_u32_e64 s[60:61], s7, v219
	s_nop 1
	v_mbcnt_lo_u32_b32 v245, s58, 0
	v_mbcnt_hi_u32_b32 v245, s59, v245
	v_cmp_gt_i32_e64 s[62:63], s9, v245
	s_bcnt1_i32_b64 s20, s[58:59]
	s_and_b64 s[62:63], s[62:63], s[58:59]
	s_or_b64 s[62:63], s[62:63], s[60:61]
	s_sub_i32 s9, s9, s20
	v_writelane_b32 v2, s62, 19
	v_writelane_b32 v3, s63, 19
	s_cmp_lt_u32 s3, 20
	s_cbranch_scc1 .Lsel_fta_done_20
	v_cmp_eq_u32_e64 s[58:59], s7, v220
	v_cmp_lt_u32_e64 s[60:61], s7, v220
	s_nop 1
	v_mbcnt_lo_u32_b32 v245, s58, 0
	v_mbcnt_hi_u32_b32 v245, s59, v245
	v_cmp_gt_i32_e64 s[62:63], s9, v245
	s_bcnt1_i32_b64 s20, s[58:59]
	s_and_b64 s[62:63], s[62:63], s[58:59]
	s_or_b64 s[62:63], s[62:63], s[60:61]
	s_sub_i32 s9, s9, s20
	v_writelane_b32 v2, s62, 20
	v_writelane_b32 v3, s63, 20
	v_cmp_eq_u32_e64 s[58:59], s7, v221
	v_cmp_lt_u32_e64 s[60:61], s7, v221
	s_nop 1
	v_mbcnt_lo_u32_b32 v245, s58, 0
	v_mbcnt_hi_u32_b32 v245, s59, v245
	v_cmp_gt_i32_e64 s[62:63], s9, v245
	s_bcnt1_i32_b64 s20, s[58:59]
	s_and_b64 s[62:63], s[62:63], s[58:59]
	s_or_b64 s[62:63], s[62:63], s[60:61]
	s_sub_i32 s9, s9, s20
	v_writelane_b32 v2, s62, 21
	v_writelane_b32 v3, s63, 21
	v_cmp_eq_u32_e64 s[58:59], s7, v222
	v_cmp_lt_u32_e64 s[60:61], s7, v222
	s_nop 1
	v_mbcnt_lo_u32_b32 v245, s58, 0
	v_mbcnt_hi_u32_b32 v245, s59, v245
	v_cmp_gt_i32_e64 s[62:63], s9, v245
	s_bcnt1_i32_b64 s20, s[58:59]
	s_and_b64 s[62:63], s[62:63], s[58:59]
	s_or_b64 s[62:63], s[62:63], s[60:61]
	s_sub_i32 s9, s9, s20
	v_writelane_b32 v2, s62, 22
	v_writelane_b32 v3, s63, 22
	v_cmp_eq_u32_e64 s[58:59], s7, v223
	v_cmp_lt_u32_e64 s[60:61], s7, v223
	s_nop 1
	v_mbcnt_lo_u32_b32 v245, s58, 0
	v_mbcnt_hi_u32_b32 v245, s59, v245
	v_cmp_gt_i32_e64 s[62:63], s9, v245
	s_bcnt1_i32_b64 s20, s[58:59]
	s_and_b64 s[62:63], s[62:63], s[58:59]
	s_or_b64 s[62:63], s[62:63], s[60:61]
	s_sub_i32 s9, s9, s20
	v_writelane_b32 v2, s62, 23
	v_writelane_b32 v3, s63, 23
	s_cmp_lt_u32 s3, 24
	s_cbranch_scc1 .Lsel_fta_done_20
	v_cmp_eq_u32_e64 s[58:59], s7, v224
	v_cmp_lt_u32_e64 s[60:61], s7, v224
	s_nop 1
	v_mbcnt_lo_u32_b32 v245, s58, 0
	v_mbcnt_hi_u32_b32 v245, s59, v245
	v_cmp_gt_i32_e64 s[62:63], s9, v245
	s_bcnt1_i32_b64 s20, s[58:59]
	s_and_b64 s[62:63], s[62:63], s[58:59]
	s_or_b64 s[62:63], s[62:63], s[60:61]
	s_sub_i32 s9, s9, s20
	v_writelane_b32 v2, s62, 24
	v_writelane_b32 v3, s63, 24
	v_cmp_eq_u32_e64 s[58:59], s7, v225
	v_cmp_lt_u32_e64 s[60:61], s7, v225
	s_nop 1
	v_mbcnt_lo_u32_b32 v245, s58, 0
	v_mbcnt_hi_u32_b32 v245, s59, v245
	v_cmp_gt_i32_e64 s[62:63], s9, v245
	s_bcnt1_i32_b64 s20, s[58:59]
	s_and_b64 s[62:63], s[62:63], s[58:59]
	s_or_b64 s[62:63], s[62:63], s[60:61]
	s_sub_i32 s9, s9, s20
	v_writelane_b32 v2, s62, 25
	v_writelane_b32 v3, s63, 25
	v_cmp_eq_u32_e64 s[58:59], s7, v226
	v_cmp_lt_u32_e64 s[60:61], s7, v226
	s_nop 1
	v_mbcnt_lo_u32_b32 v245, s58, 0
	v_mbcnt_hi_u32_b32 v245, s59, v245
	v_cmp_gt_i32_e64 s[62:63], s9, v245
	s_bcnt1_i32_b64 s20, s[58:59]
	s_and_b64 s[62:63], s[62:63], s[58:59]
	s_or_b64 s[62:63], s[62:63], s[60:61]
	s_sub_i32 s9, s9, s20
	v_writelane_b32 v2, s62, 26
	v_writelane_b32 v3, s63, 26
	v_cmp_eq_u32_e64 s[58:59], s7, v227
	v_cmp_lt_u32_e64 s[60:61], s7, v227
	s_nop 1
	v_mbcnt_lo_u32_b32 v245, s58, 0
	v_mbcnt_hi_u32_b32 v245, s59, v245
	v_cmp_gt_i32_e64 s[62:63], s9, v245
	s_bcnt1_i32_b64 s20, s[58:59]
	s_and_b64 s[62:63], s[62:63], s[58:59]
	s_or_b64 s[62:63], s[62:63], s[60:61]
	s_sub_i32 s9, s9, s20
	v_writelane_b32 v2, s62, 27
	v_writelane_b32 v3, s63, 27
	s_cmp_lt_u32 s3, 28
	s_cbranch_scc1 .Lsel_fta_done_20
	v_cmp_eq_u32_e64 s[58:59], s7, v228
	v_cmp_lt_u32_e64 s[60:61], s7, v228
	s_nop 1
	v_mbcnt_lo_u32_b32 v245, s58, 0
	v_mbcnt_hi_u32_b32 v245, s59, v245
	v_cmp_gt_i32_e64 s[62:63], s9, v245
	s_bcnt1_i32_b64 s20, s[58:59]
	s_and_b64 s[62:63], s[62:63], s[58:59]
	s_or_b64 s[62:63], s[62:63], s[60:61]
	s_sub_i32 s9, s9, s20
	v_writelane_b32 v2, s62, 28
	v_writelane_b32 v3, s63, 28
	v_cmp_eq_u32_e64 s[58:59], s7, v229
	v_cmp_lt_u32_e64 s[60:61], s7, v229
	s_nop 1
	v_mbcnt_lo_u32_b32 v245, s58, 0
	v_mbcnt_hi_u32_b32 v245, s59, v245
	v_cmp_gt_i32_e64 s[62:63], s9, v245
	s_bcnt1_i32_b64 s20, s[58:59]
	s_and_b64 s[62:63], s[62:63], s[58:59]
	s_or_b64 s[62:63], s[62:63], s[60:61]
	s_sub_i32 s9, s9, s20
	v_writelane_b32 v2, s62, 29
	v_writelane_b32 v3, s63, 29
	v_cmp_eq_u32_e64 s[58:59], s7, v230
	v_cmp_lt_u32_e64 s[60:61], s7, v230
	s_nop 1
	v_mbcnt_lo_u32_b32 v245, s58, 0
	v_mbcnt_hi_u32_b32 v245, s59, v245
	v_cmp_gt_i32_e64 s[62:63], s9, v245
	s_bcnt1_i32_b64 s20, s[58:59]
	s_and_b64 s[62:63], s[62:63], s[58:59]
	s_or_b64 s[62:63], s[62:63], s[60:61]
	s_sub_i32 s9, s9, s20
	v_writelane_b32 v2, s62, 30
	v_writelane_b32 v3, s63, 30
	v_cmp_eq_u32_e64 s[58:59], s7, v231
	v_cmp_lt_u32_e64 s[60:61], s7, v231
	s_nop 1
	v_mbcnt_lo_u32_b32 v245, s58, 0
	v_mbcnt_hi_u32_b32 v245, s59, v245
	v_cmp_gt_i32_e64 s[62:63], s9, v245
	s_bcnt1_i32_b64 s20, s[58:59]
	s_and_b64 s[62:63], s[62:63], s[58:59]
	s_or_b64 s[62:63], s[62:63], s[60:61]
	s_sub_i32 s9, s9, s20
	v_writelane_b32 v2, s62, 31
	v_writelane_b32 v3, s63, 31
.Lsel_fta_done_20:
.Lsel_fina_18:
	s_cmp_lg_u32 s13, 0
	s_cbranch_scc0 .Lsel_tieb_21
	v_cmp_le_u32_e64 s[58:59], s8, v148
	v_cmp_le_u32_e64 s[60:61], s8, v149
	v_cmp_le_u32_e64 s[62:63], s8, v150
	v_cmp_le_u32_e64 s[68:69], s8, v151
	v_writelane_b32 v4, s58, 0
	v_writelane_b32 v5, s59, 0
	v_writelane_b32 v4, s60, 1
	v_writelane_b32 v5, s61, 1
	v_writelane_b32 v4, s62, 2
	v_writelane_b32 v5, s63, 2
	v_writelane_b32 v4, s68, 3
	v_writelane_b32 v5, s69, 3
	v_cmp_le_u32_e64 s[58:59], s8, v152
	v_cmp_le_u32_e64 s[60:61], s8, v153
	v_cmp_le_u32_e64 s[62:63], s8, v154
	v_cmp_le_u32_e64 s[68:69], s8, v155
	v_writelane_b32 v4, s58, 4
	v_writelane_b32 v5, s59, 4
	v_writelane_b32 v4, s60, 5
	v_writelane_b32 v5, s61, 5
	v_writelane_b32 v4, s62, 6
	v_writelane_b32 v5, s63, 6
	v_writelane_b32 v4, s68, 7
	v_writelane_b32 v5, s69, 7
	s_cmp_lt_u32 s3, 8
	s_cbranch_scc1 .Lsel_feb_done_23
	v_cmp_le_u32_e64 s[58:59], s8, v156
	v_cmp_le_u32_e64 s[60:61], s8, v157
	v_cmp_le_u32_e64 s[62:63], s8, v158
	v_cmp_le_u32_e64 s[68:69], s8, v159
	v_writelane_b32 v4, s58, 8
	v_writelane_b32 v5, s59, 8
	v_writelane_b32 v4, s60, 9
	v_writelane_b32 v5, s61, 9
	v_writelane_b32 v4, s62, 10
	v_writelane_b32 v5, s63, 10
	v_writelane_b32 v4, s68, 11
	v_writelane_b32 v5, s69, 11
	s_cmp_lt_u32 s3, 12
	s_cbranch_scc1 .Lsel_feb_done_23
	v_cmp_le_u32_e64 s[58:59], s8, v160
	v_cmp_le_u32_e64 s[60:61], s8, v161
	v_cmp_le_u32_e64 s[62:63], s8, v162
	v_cmp_le_u32_e64 s[68:69], s8, v163
	v_writelane_b32 v4, s58, 12
	v_writelane_b32 v5, s59, 12
	v_writelane_b32 v4, s60, 13
	v_writelane_b32 v5, s61, 13
	v_writelane_b32 v4, s62, 14
	v_writelane_b32 v5, s63, 14
	v_writelane_b32 v4, s68, 15
	v_writelane_b32 v5, s69, 15
	s_cmp_lt_u32 s3, 16
	s_cbranch_scc1 .Lsel_feb_done_23
	v_cmp_le_u32_e64 s[58:59], s8, v164
	v_cmp_le_u32_e64 s[60:61], s8, v165
	v_cmp_le_u32_e64 s[62:63], s8, v166
	v_cmp_le_u32_e64 s[68:69], s8, v167
	v_writelane_b32 v4, s58, 16
	v_writelane_b32 v5, s59, 16
	v_writelane_b32 v4, s60, 17
	v_writelane_b32 v5, s61, 17
	v_writelane_b32 v4, s62, 18
	v_writelane_b32 v5, s63, 18
	v_writelane_b32 v4, s68, 19
	v_writelane_b32 v5, s69, 19
	s_cmp_lt_u32 s3, 20
	s_cbranch_scc1 .Lsel_feb_done_23
	v_cmp_le_u32_e64 s[58:59], s8, v168
	v_cmp_le_u32_e64 s[60:61], s8, v169
	v_cmp_le_u32_e64 s[62:63], s8, v170
	v_cmp_le_u32_e64 s[68:69], s8, v171
	v_writelane_b32 v4, s58, 20
	v_writelane_b32 v5, s59, 20
	v_writelane_b32 v4, s60, 21
	v_writelane_b32 v5, s61, 21
	v_writelane_b32 v4, s62, 22
	v_writelane_b32 v5, s63, 22
	v_writelane_b32 v4, s68, 23
	v_writelane_b32 v5, s69, 23
	s_cmp_lt_u32 s3, 24
	s_cbranch_scc1 .Lsel_feb_done_23
	v_cmp_le_u32_e64 s[58:59], s8, v172
	v_cmp_le_u32_e64 s[60:61], s8, v173
	v_cmp_le_u32_e64 s[62:63], s8, v174
	v_cmp_le_u32_e64 s[68:69], s8, v175
	v_writelane_b32 v4, s58, 24
	v_writelane_b32 v5, s59, 24
	v_writelane_b32 v4, s60, 25
	v_writelane_b32 v5, s61, 25
	v_writelane_b32 v4, s62, 26
	v_writelane_b32 v5, s63, 26
	v_writelane_b32 v4, s68, 27
	v_writelane_b32 v5, s69, 27
	s_cmp_lt_u32 s3, 28
	s_cbranch_scc1 .Lsel_feb_done_23
	v_cmp_le_u32_e64 s[58:59], s8, v176
	v_cmp_le_u32_e64 s[60:61], s8, v177
	v_cmp_le_u32_e64 s[62:63], s8, v186
	v_cmp_le_u32_e64 s[68:69], s8, v187
	v_writelane_b32 v4, s58, 28
	v_writelane_b32 v5, s59, 28
	v_writelane_b32 v4, s60, 29
	v_writelane_b32 v5, s61, 29
	v_writelane_b32 v4, s62, 30
	v_writelane_b32 v5, s63, 30
	v_writelane_b32 v4, s68, 31
	v_writelane_b32 v5, s69, 31

.Lsel_tieb_21:
	v_cmp_eq_u32_e64 s[58:59], s8, v148
	v_cmp_lt_u32_e64 s[60:61], s8, v148
	s_nop 1
	v_mbcnt_lo_u32_b32 v245, s58, 0
	v_mbcnt_hi_u32_b32 v245, s59, v245
	v_cmp_gt_i32_e64 s[62:63], s10, v245
	s_bcnt1_i32_b64 s20, s[58:59]
	s_and_b64 s[62:63], s[62:63], s[58:59]
	s_or_b64 s[62:63], s[62:63], s[60:61]
	s_sub_i32 s10, s10, s20
	v_writelane_b32 v4, s62, 0
	v_writelane_b32 v5, s63, 0
	v_cmp_eq_u32_e64 s[58:59], s8, v149
	v_cmp_lt_u32_e64 s[60:61], s8, v149
	s_nop 1
	v_mbcnt_lo_u32_b32 v245, s58, 0
	v_mbcnt_hi_u32_b32 v245, s59, v245
	v_cmp_gt_i32_e64 s[62:63], s10, v245
	s_bcnt1_i32_b64 s20, s[58:59]
	s_and_b64 s[62:63], s[62:63], s[58:59]
	s_or_b64 s[62:63], s[62:63], s[60:61]
	s_sub_i32 s10, s10, s20
	v_writelane_b32 v4, s62, 1
	v_writelane_b32 v5, s63, 1
	v_cmp_eq_u32_e64 s[58:59], s8, v150
	v_cmp_lt_u32_e64 s[60:61], s8, v150
	s_nop 1
	v_mbcnt_lo_u32_b32 v245, s58, 0
	v_mbcnt_hi_u32_b32 v245, s59, v245
	v_cmp_gt_i32_e64 s[62:63], s10, v245
	s_bcnt1_i32_b64 s20, s[58:59]
	s_and_b64 s[62:63], s[62:63], s[58:59]
	s_or_b64 s[62:63], s[62:63], s[60:61]
	s_sub_i32 s10, s10, s20
	v_writelane_b32 v4, s62, 2
	v_writelane_b32 v5, s63, 2
	v_cmp_eq_u32_e64 s[58:59], s8, v151
	v_cmp_lt_u32_e64 s[60:61], s8, v151
	s_nop 1
	v_mbcnt_lo_u32_b32 v245, s58, 0
	v_mbcnt_hi_u32_b32 v245, s59, v245
	v_cmp_gt_i32_e64 s[62:63], s10, v245
	s_bcnt1_i32_b64 s20, s[58:59]
	s_and_b64 s[62:63], s[62:63], s[58:59]
	s_or_b64 s[62:63], s[62:63], s[60:61]
	s_sub_i32 s10, s10, s20
	v_writelane_b32 v4, s62, 3
	v_writelane_b32 v5, s63, 3
	v_cmp_eq_u32_e64 s[58:59], s8, v152
	v_cmp_lt_u32_e64 s[60:61], s8, v152
	s_nop 1
	v_mbcnt_lo_u32_b32 v245, s58, 0
	v_mbcnt_hi_u32_b32 v245, s59, v245
	v_cmp_gt_i32_e64 s[62:63], s10, v245
	s_bcnt1_i32_b64 s20, s[58:59]
	s_and_b64 s[62:63], s[62:63], s[58:59]
	s_or_b64 s[62:63], s[62:63], s[60:61]
	s_sub_i32 s10, s10, s20
	v_writelane_b32 v4, s62, 4
	v_writelane_b32 v5, s63, 4
	v_cmp_eq_u32_e64 s[58:59], s8, v153
	v_cmp_lt_u32_e64 s[60:61], s8, v153
	s_nop 1
	v_mbcnt_lo_u32_b32 v245, s58, 0
	v_mbcnt_hi_u32_b32 v245, s59, v245
	v_cmp_gt_i32_e64 s[62:63], s10, v245
	s_bcnt1_i32_b64 s20, s[58:59]
	s_and_b64 s[62:63], s[62:63], s[58:59]
	s_or_b64 s[62:63], s[62:63], s[60:61]
	s_sub_i32 s10, s10, s20
	v_writelane_b32 v4, s62, 5
	v_writelane_b32 v5, s63, 5
	v_cmp_eq_u32_e64 s[58:59], s8, v154
	v_cmp_lt_u32_e64 s[60:61], s8, v154
	s_nop 1
	v_mbcnt_lo_u32_b32 v245, s58, 0
	v_mbcnt_hi_u32_b32 v245, s59, v245
	v_cmp_gt_i32_e64 s[62:63], s10, v245
	s_bcnt1_i32_b64 s20, s[58:59]
	s_and_b64 s[62:63], s[62:63], s[58:59]
	s_or_b64 s[62:63], s[62:63], s[60:61]
	s_sub_i32 s10, s10, s20
	v_writelane_b32 v4, s62, 6
	v_writelane_b32 v5, s63, 6
	v_cmp_eq_u32_e64 s[58:59], s8, v155
	v_cmp_lt_u32_e64 s[60:61], s8, v155
	s_nop 1
	v_mbcnt_lo_u32_b32 v245, s58, 0
	v_mbcnt_hi_u32_b32 v245, s59, v245
	v_cmp_gt_i32_e64 s[62:63], s10, v245
	s_bcnt1_i32_b64 s20, s[58:59]
	s_and_b64 s[62:63], s[62:63], s[58:59]
	s_or_b64 s[62:63], s[62:63], s[60:61]
	s_sub_i32 s10, s10, s20
	v_writelane_b32 v4, s62, 7
	v_writelane_b32 v5, s63, 7
	s_cmp_lt_u32 s3, 8
	s_cbranch_scc1 .Lsel_ftb_done_24
	v_cmp_eq_u32_e64 s[58:59], s8, v156
	v_cmp_lt_u32_e64 s[60:61], s8, v156
	s_nop 1
	v_mbcnt_lo_u32_b32 v245, s58, 0
	v_mbcnt_hi_u32_b32 v245, s59, v245
	v_cmp_gt_i32_e64 s[62:63], s10, v245
	s_bcnt1_i32_b64 s20, s[58:59]
	s_and_b64 s[62:63], s[62:63], s[58:59]
	s_or_b64 s[62:63], s[62:63], s[60:61]
	s_sub_i32 s10, s10, s20
	v_writelane_b32 v4, s62, 8
	v_writelane_b32 v5, s63, 8
	v_cmp_eq_u32_e64 s[58:59], s8, v157
	v_cmp_lt_u32_e64 s[60:61], s8, v157
	s_nop 1
	v_mbcnt_lo_u32_b32 v245, s58, 0
	v_mbcnt_hi_u32_b32 v245, s59, v245
	v_cmp_gt_i32_e64 s[62:63], s10, v245
	s_bcnt1_i32_b64 s20, s[58:59]
	s_and_b64 s[62:63], s[62:63], s[58:59]
	s_or_b64 s[62:63], s[62:63], s[60:61]
	s_sub_i32 s10, s10, s20
	v_writelane_b32 v4, s62, 9
	v_writelane_b32 v5, s63, 9
	v_cmp_eq_u32_e64 s[58:59], s8, v158
	v_cmp_lt_u32_e64 s[60:61], s8, v158
	s_nop 1
	v_mbcnt_lo_u32_b32 v245, s58, 0
	v_mbcnt_hi_u32_b32 v245, s59, v245
	v_cmp_gt_i32_e64 s[62:63], s10, v245
	s_bcnt1_i32_b64 s20, s[58:59]
	s_and_b64 s[62:63], s[62:63], s[58:59]
	s_or_b64 s[62:63], s[62:63], s[60:61]
	s_sub_i32 s10, s10, s20
	v_writelane_b32 v4, s62, 10
	v_writelane_b32 v5, s63, 10
	v_cmp_eq_u32_e64 s[58:59], s8, v159
	v_cmp_lt_u32_e64 s[60:61], s8, v159
	s_nop 1
	v_mbcnt_lo_u32_b32 v245, s58, 0
	v_mbcnt_hi_u32_b32 v245, s59, v245
	v_cmp_gt_i32_e64 s[62:63], s10, v245
	s_bcnt1_i32_b64 s20, s[58:59]
	s_and_b64 s[62:63], s[62:63], s[58:59]
	s_or_b64 s[62:63], s[62:63], s[60:61]
	s_sub_i32 s10, s10, s20
	v_writelane_b32 v4, s62, 11
	v_writelane_b32 v5, s63, 11
	s_cmp_lt_u32 s3, 12
	s_cbranch_scc1 .Lsel_ftb_done_24
	v_cmp_eq_u32_e64 s[58:59], s8, v160
	v_cmp_lt_u32_e64 s[60:61], s8, v160
	s_nop 1
	v_mbcnt_lo_u32_b32 v245, s58, 0
	v_mbcnt_hi_u32_b32 v245, s59, v245
	v_cmp_gt_i32_e64 s[62:63], s10, v245
	s_bcnt1_i32_b64 s20, s[58:59]
	s_and_b64 s[62:63], s[62:63], s[58:59]
	s_or_b64 s[62:63], s[62:63], s[60:61]
	s_sub_i32 s10, s10, s20
	v_writelane_b32 v4, s62, 12
	v_writelane_b32 v5, s63, 12
	v_cmp_eq_u32_e64 s[58:59], s8, v161
	v_cmp_lt_u32_e64 s[60:61], s8, v161
	s_nop 1
	v_mbcnt_lo_u32_b32 v245, s58, 0
	v_mbcnt_hi_u32_b32 v245, s59, v245
	v_cmp_gt_i32_e64 s[62:63], s10, v245
	s_bcnt1_i32_b64 s20, s[58:59]
	s_and_b64 s[62:63], s[62:63], s[58:59]
	s_or_b64 s[62:63], s[62:63], s[60:61]
	s_sub_i32 s10, s10, s20
	v_writelane_b32 v4, s62, 13
	v_writelane_b32 v5, s63, 13
	v_cmp_eq_u32_e64 s[58:59], s8, v162
	v_cmp_lt_u32_e64 s[60:61], s8, v162
	s_nop 1
	v_mbcnt_lo_u32_b32 v245, s58, 0
	v_mbcnt_hi_u32_b32 v245, s59, v245
	v_cmp_gt_i32_e64 s[62:63], s10, v245
	s_bcnt1_i32_b64 s20, s[58:59]
	s_and_b64 s[62:63], s[62:63], s[58:59]
	s_or_b64 s[62:63], s[62:63], s[60:61]
	s_sub_i32 s10, s10, s20
	v_writelane_b32 v4, s62, 14
	v_writelane_b32 v5, s63, 14
	v_cmp_eq_u32_e64 s[58:59], s8, v163
	v_cmp_lt_u32_e64 s[60:61], s8, v163
	s_nop 1
	v_mbcnt_lo_u32_b32 v245, s58, 0
	v_mbcnt_hi_u32_b32 v245, s59, v245
	v_cmp_gt_i32_e64 s[62:63], s10, v245
	s_bcnt1_i32_b64 s20, s[58:59]
	s_and_b64 s[62:63], s[62:63], s[58:59]
	s_or_b64 s[62:63], s[62:63], s[60:61]
	s_sub_i32 s10, s10, s20
	v_writelane_b32 v4, s62, 15
	v_writelane_b32 v5, s63, 15
	s_cmp_lt_u32 s3, 16
	s_cbranch_scc1 .Lsel_ftb_done_24
	v_cmp_eq_u32_e64 s[58:59], s8, v164
	v_cmp_lt_u32_e64 s[60:61], s8, v164
	s_nop 1
	v_mbcnt_lo_u32_b32 v245, s58, 0
	v_mbcnt_hi_u32_b32 v245, s59, v245
	v_cmp_gt_i32_e64 s[62:63], s10, v245
	s_bcnt1_i32_b64 s20, s[58:59]
	s_and_b64 s[62:63], s[62:63], s[58:59]
	s_or_b64 s[62:63], s[62:63], s[60:61]
	s_sub_i32 s10, s10, s20
	v_writelane_b32 v4, s62, 16
	v_writelane_b32 v5, s63, 16
	v_cmp_eq_u32_e64 s[58:59], s8, v165
	v_cmp_lt_u32_e64 s[60:61], s8, v165
	s_nop 1
	v_mbcnt_lo_u32_b32 v245, s58, 0
	v_mbcnt_hi_u32_b32 v245, s59, v245
	v_cmp_gt_i32_e64 s[62:63], s10, v245
	s_bcnt1_i32_b64 s20, s[58:59]
	s_and_b64 s[62:63], s[62:63], s[58:59]
	s_or_b64 s[62:63], s[62:63], s[60:61]
	s_sub_i32 s10, s10, s20
	v_writelane_b32 v4, s62, 17
	v_writelane_b32 v5, s63, 17
	v_cmp_eq_u32_e64 s[58:59], s8, v166
	v_cmp_lt_u32_e64 s[60:61], s8, v166
	s_nop 1
	v_mbcnt_lo_u32_b32 v245, s58, 0
	v_mbcnt_hi_u32_b32 v245, s59, v245
	v_cmp_gt_i32_e64 s[62:63], s10, v245
	s_bcnt1_i32_b64 s20, s[58:59]
	s_and_b64 s[62:63], s[62:63], s[58:59]
	s_or_b64 s[62:63], s[62:63], s[60:61]
	s_sub_i32 s10, s10, s20
	v_writelane_b32 v4, s62, 18
	v_writelane_b32 v5, s63, 18
	v_cmp_eq_u32_e64 s[58:59], s8, v167
	v_cmp_lt_u32_e64 s[60:61], s8, v167
	s_nop 1
	v_mbcnt_lo_u32_b32 v245, s58, 0
	v_mbcnt_hi_u32_b32 v245, s59, v245
	v_cmp_gt_i32_e64 s[62:63], s10, v245
	s_bcnt1_i32_b64 s20, s[58:59]
	s_and_b64 s[62:63], s[62:63], s[58:59]
	s_or_b64 s[62:63], s[62:63], s[60:61]
	s_sub_i32 s10, s10, s20
	v_writelane_b32 v4, s62, 19
	v_writelane_b32 v5, s63, 19
	s_cmp_lt_u32 s3, 20
	s_cbranch_scc1 .Lsel_ftb_done_24
	v_cmp_eq_u32_e64 s[58:59], s8, v168
	v_cmp_lt_u32_e64 s[60:61], s8, v168
	s_nop 1
	v_mbcnt_lo_u32_b32 v245, s58, 0
	v_mbcnt_hi_u32_b32 v245, s59, v245
	v_cmp_gt_i32_e64 s[62:63], s10, v245
	s_bcnt1_i32_b64 s20, s[58:59]
	s_and_b64 s[62:63], s[62:63], s[58:59]
	s_or_b64 s[62:63], s[62:63], s[60:61]
	s_sub_i32 s10, s10, s20
	v_writelane_b32 v4, s62, 20
	v_writelane_b32 v5, s63, 20
	v_cmp_eq_u32_e64 s[58:59], s8, v169
	v_cmp_lt_u32_e64 s[60:61], s8, v169
	s_nop 1
	v_mbcnt_lo_u32_b32 v245, s58, 0
	v_mbcnt_hi_u32_b32 v245, s59, v245
	v_cmp_gt_i32_e64 s[62:63], s10, v245
	s_bcnt1_i32_b64 s20, s[58:59]
	s_and_b64 s[62:63], s[62:63], s[58:59]
	s_or_b64 s[62:63], s[62:63], s[60:61]
	s_sub_i32 s10, s10, s20
	v_writelane_b32 v4, s62, 21
	v_writelane_b32 v5, s63, 21
	v_cmp_eq_u32_e64 s[58:59], s8, v170
	v_cmp_lt_u32_e64 s[60:61], s8, v170
	s_nop 1
	v_mbcnt_lo_u32_b32 v245, s58, 0
	v_mbcnt_hi_u32_b32 v245, s59, v245
	v_cmp_gt_i32_e64 s[62:63], s10, v245
	s_bcnt1_i32_b64 s20, s[58:59]
	s_and_b64 s[62:63], s[62:63], s[58:59]
	s_or_b64 s[62:63], s[62:63], s[60:61]
	s_sub_i32 s10, s10, s20
	v_writelane_b32 v4, s62, 22
	v_writelane_b32 v5, s63, 22
	v_cmp_eq_u32_e64 s[58:59], s8, v171
	v_cmp_lt_u32_e64 s[60:61], s8, v171
	s_nop 1
	v_mbcnt_lo_u32_b32 v245, s58, 0
	v_mbcnt_hi_u32_b32 v245, s59, v245
	v_cmp_gt_i32_e64 s[62:63], s10, v245
	s_bcnt1_i32_b64 s20, s[58:59]
	s_and_b64 s[62:63], s[62:63], s[58:59]
	s_or_b64 s[62:63], s[62:63], s[60:61]
	s_sub_i32 s10, s10, s20
	v_writelane_b32 v4, s62, 23
	v_writelane_b32 v5, s63, 23
	s_cmp_lt_u32 s3, 24
	s_cbranch_scc1 .Lsel_ftb_done_24
	v_cmp_eq_u32_e64 s[58:59], s8, v172
	v_cmp_lt_u32_e64 s[60:61], s8, v172
	s_nop 1
	v_mbcnt_lo_u32_b32 v245, s58, 0
	v_mbcnt_hi_u32_b32 v245, s59, v245
	v_cmp_gt_i32_e64 s[62:63], s10, v245
	s_bcnt1_i32_b64 s20, s[58:59]
	s_and_b64 s[62:63], s[62:63], s[58:59]
	s_or_b64 s[62:63], s[62:63], s[60:61]
	s_sub_i32 s10, s10, s20
	v_writelane_b32 v4, s62, 24
	v_writelane_b32 v5, s63, 24
	v_cmp_eq_u32_e64 s[58:59], s8, v173
	v_cmp_lt_u32_e64 s[60:61], s8, v173
	s_nop 1
	v_mbcnt_lo_u32_b32 v245, s58, 0
	v_mbcnt_hi_u32_b32 v245, s59, v245
	v_cmp_gt_i32_e64 s[62:63], s10, v245
	s_bcnt1_i32_b64 s20, s[58:59]
	s_and_b64 s[62:63], s[62:63], s[58:59]
	s_or_b64 s[62:63], s[62:63], s[60:61]
	s_sub_i32 s10, s10, s20
	v_writelane_b32 v4, s62, 25
	v_writelane_b32 v5, s63, 25
	v_cmp_eq_u32_e64 s[58:59], s8, v174
	v_cmp_lt_u32_e64 s[60:61], s8, v174
	s_nop 1
	v_mbcnt_lo_u32_b32 v245, s58, 0
	v_mbcnt_hi_u32_b32 v245, s59, v245
	v_cmp_gt_i32_e64 s[62:63], s10, v245
	s_bcnt1_i32_b64 s20, s[58:59]
	s_and_b64 s[62:63], s[62:63], s[58:59]
	s_or_b64 s[62:63], s[62:63], s[60:61]
	s_sub_i32 s10, s10, s20
	v_writelane_b32 v4, s62, 26
	v_writelane_b32 v5, s63, 26
	v_cmp_eq_u32_e64 s[58:59], s8, v175
	v_cmp_lt_u32_e64 s[60:61], s8, v175
	s_nop 1
	v_mbcnt_lo_u32_b32 v245, s58, 0
	v_mbcnt_hi_u32_b32 v245, s59, v245
	v_cmp_gt_i32_e64 s[62:63], s10, v245
	s_bcnt1_i32_b64 s20, s[58:59]
	s_and_b64 s[62:63], s[62:63], s[58:59]
	s_or_b64 s[62:63], s[62:63], s[60:61]
	s_sub_i32 s10, s10, s20
	v_writelane_b32 v4, s62, 27
	v_writelane_b32 v5, s63, 27
	s_cmp_lt_u32 s3, 28
	s_cbranch_scc1 .Lsel_ftb_done_24
	v_cmp_eq_u32_e64 s[58:59], s8, v176
	v_cmp_lt_u32_e64 s[60:61], s8, v176
	s_nop 1
	v_mbcnt_lo_u32_b32 v245, s58, 0
	v_mbcnt_hi_u32_b32 v245, s59, v245
	v_cmp_gt_i32_e64 s[62:63], s10, v245
	s_bcnt1_i32_b64 s20, s[58:59]
	s_and_b64 s[62:63], s[62:63], s[58:59]
	s_or_b64 s[62:63], s[62:63], s[60:61]
	s_sub_i32 s10, s10, s20
	v_writelane_b32 v4, s62, 28
	v_writelane_b32 v5, s63, 28
	v_cmp_eq_u32_e64 s[58:59], s8, v177
	v_cmp_lt_u32_e64 s[60:61], s8, v177
	s_nop 1
	v_mbcnt_lo_u32_b32 v245, s58, 0
	v_mbcnt_hi_u32_b32 v245, s59, v245
	v_cmp_gt_i32_e64 s[62:63], s10, v245
	s_bcnt1_i32_b64 s20, s[58:59]
	s_and_b64 s[62:63], s[62:63], s[58:59]
	s_or_b64 s[62:63], s[62:63], s[60:61]
	s_sub_i32 s10, s10, s20
	v_writelane_b32 v4, s62, 29
	v_writelane_b32 v5, s63, 29
	v_cmp_eq_u32_e64 s[58:59], s8, v186
	v_cmp_lt_u32_e64 s[60:61], s8, v186
	s_nop 1
	v_mbcnt_lo_u32_b32 v245, s58, 0
	v_mbcnt_hi_u32_b32 v245, s59, v245
	v_cmp_gt_i32_e64 s[62:63], s10, v245
	s_bcnt1_i32_b64 s20, s[58:59]
	s_and_b64 s[62:63], s[62:63], s[58:59]
	s_or_b64 s[62:63], s[62:63], s[60:61]
	s_sub_i32 s10, s10, s20
	v_writelane_b32 v4, s62, 30
	v_writelane_b32 v5, s63, 30
	v_cmp_eq_u32_e64 s[58:59], s8, v187
	v_cmp_lt_u32_e64 s[60:61], s8, v187
	s_nop 1
	v_mbcnt_lo_u32_b32 v245, s58, 0
	v_mbcnt_hi_u32_b32 v245, s59, v245
	v_cmp_gt_i32_e64 s[62:63], s10, v245
	s_bcnt1_i32_b64 s20, s[58:59]
	s_and_b64 s[62:63], s[62:63], s[58:59]
	s_or_b64 s[62:63], s[62:63], s[60:61]
	s_sub_i32 s10, s10, s20
	v_writelane_b32 v4, s62, 31
	v_writelane_b32 v5, s63, 31
.Lsel_ftb_done_24:
.Lsel_finb_22:
	s_branch .LBB0_1237
.LBB0_602:
	s_and_b64 vcc, exec, s[0:1]
	s_cbranch_vccz .LBB0_1237
	v_lshlrev_b32_e32 v4, 6, v146
	v_add_u32_e32 v6, 64, v4
	v_sub_u32_e32 v2, s22, v4
	v_cmp_lt_u32_e32 vcc, s92, v4
	v_sub_u32_e32 v4, s31, v4
	v_lshlrev_b64 v[2:3], v2, -1
	v_lshlrev_b64 v[4:5], v4, -1
	v_not_b32_e32 v3, v3
	v_not_b32_e32 v2, v2
	v_not_b32_e32 v5, v5
	v_not_b32_e32 v4, v4
	v_cndmask_b32_e64 v2, v2, 0, vcc
	v_cndmask_b32_e64 v3, v3, 0, vcc
	v_cmp_lt_u32_e64 s[4:5], s22, v6
	v_cndmask_b32_e64 v4, v4, 0, vcc
	v_cndmask_b32_e64 v5, v5, 0, vcc
	v_cmp_lt_u32_e32 vcc, s31, v6
	v_cndmask_b32_e64 v3, -1, v3, s[4:5]
	v_cndmask_b32_e64 v2, -1, v2, s[4:5]
	v_cndmask_b32_e32 v5, -1, v5, vcc
	v_cndmask_b32_e32 v4, -1, v4, vcc
	v_cmp_gt_u32_e32 vcc, 32, v146
	s_and_saveexec_b64 s[0:1], vcc
	s_cbranch_execz .LBB0_566
	s_branch .LBB0_1238
.LBB0_1236:
.LBB0_1237:
	v_cmp_gt_u32_e32 vcc, 32, v146
	s_and_saveexec_b64 s[0:1], vcc
	s_cbranch_execz .LBB0_566
